# v43 + one barrier per tile pair (5-buffer LDS ring)
# baseline (speedup 1.0000x reference)
.LBB1_235:
	v_mov_b32_e32 v110, v18
	v_mov_b32_e32 v111, v19
	v_mov_b32_e32 v112, v20
	v_mov_b32_e32 v113, v21
	s_mov_b32 s72, 0x2000
	s_mov_b32 s73, 0
	s_mov_b32 s74, 0x20000
	s_mov_b32 s75, 0
	v_lshl_add_u64 v[158:159], v[158:159], 0, s[74:75]
	v_mul_u32_u24_e32 v163, 0x110, v160
	v_lshl_add_u32 v162, v1, 4, v163
	v_add_u32_e32 v163, 0x11000, v162
	global_load_dwordx4 v[94:97], v[158:159], off
	v_lshl_add_u64 v[158:159], v[158:159], 0, s[72:73]
	global_load_dwordx4 v[98:101], v[158:159], off
	v_lshl_add_u64 v[158:159], v[158:159], 0, s[72:73]
	global_load_dwordx4 v[102:105], v[158:159], off
	v_lshl_add_u64 v[158:159], v[158:159], 0, s[72:73]
	global_load_dwordx4 v[106:109], v[158:159], off
	v_lshl_add_u64 v[158:159], v[158:159], 0, s[72:73]
	global_load_dwordx4 v[142:145], v[158:159], off
	v_lshl_add_u64 v[158:159], v[158:159], 0, s[72:73]
	global_load_dwordx4 v[146:149], v[158:159], off
	v_lshl_add_u64 v[158:159], v[158:159], 0, s[72:73]
	global_load_dwordx4 v[150:153], v[158:159], off
	v_lshl_add_u64 v[158:159], v[158:159], 0, s[72:73]
	global_load_dwordx4 v[154:157], v[158:159], off
	v_lshl_add_u64 v[158:159], v[158:159], 0, s[72:73]
	s_waitcnt lgkmcnt(0)
	s_barrier
	ds_read_b128 v[114:117], v162 offset:0
	ds_read_b128 v[118:121], v162 offset:8704
	ds_read_b128 v[122:125], v162 offset:32
	ds_read_b128 v[126:129], v162 offset:8736
	ds_read_b128 v[130:133], v162 offset:64
	ds_read_b128 v[134:137], v162 offset:8768
	s_waitcnt lgkmcnt(5)
	v_mfma_f32_32x32x16_f16 v[2:17], v[114:117], v[110:113], 0
	s_waitcnt lgkmcnt(4)
	v_mfma_f32_32x32x16_f16 v[18:33], v[118:121], v[110:113], 0
	ds_read_b128 v[114:117], v162 offset:96
	ds_read_b128 v[118:121], v162 offset:8800
	global_load_dwordx4 v[110:113], v[158:159], off
	v_lshl_add_u64 v[158:159], v[158:159], 0, s[72:73]
	s_waitcnt lgkmcnt(5)
	v_mfma_f32_32x32x16_f16 v[2:17], v[122:125], v[90:93], v[2:17]
	s_waitcnt lgkmcnt(4)
	v_mfma_f32_32x32x16_f16 v[18:33], v[126:129], v[90:93], v[18:33]
	ds_read_b128 v[122:125], v162 offset:128
	ds_read_b128 v[126:129], v162 offset:8832
	global_load_dwordx4 v[90:93], v[158:159], off
	v_lshl_add_u64 v[158:159], v[158:159], 0, s[72:73]
	s_waitcnt lgkmcnt(5)
	v_mfma_f32_32x32x16_f16 v[2:17], v[130:133], v[86:89], v[2:17]
	s_waitcnt lgkmcnt(4)
	v_mfma_f32_32x32x16_f16 v[18:33], v[134:137], v[86:89], v[18:33]
	ds_read_b128 v[130:133], v162 offset:160
	ds_read_b128 v[134:137], v162 offset:8864
	global_load_dwordx4 v[86:89], v[158:159], off
	v_lshl_add_u64 v[158:159], v[158:159], 0, s[72:73]
	s_waitcnt lgkmcnt(5)
	v_mfma_f32_32x32x16_f16 v[2:17], v[114:117], v[82:85], v[2:17]
	s_waitcnt lgkmcnt(4)
	v_mfma_f32_32x32x16_f16 v[18:33], v[118:121], v[82:85], v[18:33]
	ds_read_b128 v[114:117], v162 offset:192
	ds_read_b128 v[118:121], v162 offset:8896
	global_load_dwordx4 v[82:85], v[158:159], off
	v_lshl_add_u64 v[158:159], v[158:159], 0, s[72:73]
	s_waitcnt lgkmcnt(5)
	v_mfma_f32_32x32x16_f16 v[2:17], v[122:125], v[78:81], v[2:17]
	s_waitcnt lgkmcnt(4)
	v_mfma_f32_32x32x16_f16 v[18:33], v[126:129], v[78:81], v[18:33]
	ds_read_b128 v[122:125], v162 offset:224
	ds_read_b128 v[126:129], v162 offset:8928
	global_load_dwordx4 v[78:81], v[158:159], off
	v_lshl_add_u64 v[158:159], v[158:159], 0, s[72:73]
	s_waitcnt lgkmcnt(5)
	v_mfma_f32_32x32x16_f16 v[2:17], v[130:133], v[74:77], v[2:17]
	s_waitcnt lgkmcnt(4)
	v_mfma_f32_32x32x16_f16 v[18:33], v[134:137], v[74:77], v[18:33]
	global_load_dwordx4 v[74:77], v[158:159], off
	v_lshl_add_u64 v[158:159], v[158:159], 0, s[72:73]
	s_waitcnt lgkmcnt(3)
	v_mfma_f32_32x32x16_f16 v[2:17], v[114:117], v[70:73], v[2:17]
	s_waitcnt lgkmcnt(2)
	v_mfma_f32_32x32x16_f16 v[18:33], v[118:121], v[70:73], v[18:33]
	global_load_dwordx4 v[70:73], v[158:159], off
	v_lshl_add_u64 v[158:159], v[158:159], 0, s[72:73]
	s_waitcnt lgkmcnt(1)
	v_mfma_f32_32x32x16_f16 v[2:17], v[122:125], v[66:69], v[2:17]
	s_waitcnt lgkmcnt(0)
	v_mfma_f32_32x32x16_f16 v[18:33], v[126:129], v[66:69], v[18:33]
	global_load_dwordx4 v[66:69], v[158:159], off
	v_lshl_add_u64 v[158:159], v[158:159], 0, s[72:73]
	ds_read_b128 v[114:117], v162 offset:17408
	ds_read_b128 v[118:121], v162 offset:26112
	ds_read_b128 v[122:125], v162 offset:17440
	ds_read_b128 v[126:129], v162 offset:26144
	ds_read_b128 v[130:133], v162 offset:17472
	ds_read_b128 v[134:137], v162 offset:26176
	s_waitcnt lgkmcnt(5)
	v_mfma_f32_32x32x16_f16 v[2:17], v[114:117], v[62:65], v[2:17]
	s_waitcnt lgkmcnt(4)
	v_mfma_f32_32x32x16_f16 v[18:33], v[118:121], v[62:65], v[18:33]
	ds_read_b128 v[114:117], v162 offset:17504
	ds_read_b128 v[118:121], v162 offset:26208
	global_load_dwordx4 v[62:65], v[158:159], off
	v_lshl_add_u64 v[158:159], v[158:159], 0, s[72:73]
	s_waitcnt lgkmcnt(5)
	v_mfma_f32_32x32x16_f16 v[2:17], v[122:125], v[58:61], v[2:17]
	s_waitcnt lgkmcnt(4)
	v_mfma_f32_32x32x16_f16 v[18:33], v[126:129], v[58:61], v[18:33]
	ds_read_b128 v[122:125], v162 offset:17536
	ds_read_b128 v[126:129], v162 offset:26240
	global_load_dwordx4 v[58:61], v[158:159], off
	v_lshl_add_u64 v[158:159], v[158:159], 0, s[72:73]
	s_waitcnt lgkmcnt(5)
	v_mfma_f32_32x32x16_f16 v[2:17], v[130:133], v[54:57], v[2:17]
	s_waitcnt lgkmcnt(4)
	v_mfma_f32_32x32x16_f16 v[18:33], v[134:137], v[54:57], v[18:33]
	ds_read_b128 v[130:133], v162 offset:17568
	ds_read_b128 v[134:137], v162 offset:26272
	global_load_dwordx4 v[54:57], v[158:159], off
	v_lshl_add_u64 v[158:159], v[158:159], 0, s[72:73]
	s_waitcnt lgkmcnt(5)
	v_mfma_f32_32x32x16_f16 v[2:17], v[114:117], v[50:53], v[2:17]
	s_waitcnt lgkmcnt(4)
	v_mfma_f32_32x32x16_f16 v[18:33], v[118:121], v[50:53], v[18:33]
	ds_read_b128 v[114:117], v162 offset:17600
	ds_read_b128 v[118:121], v162 offset:26304
	global_load_dwordx4 v[50:53], v[158:159], off
	v_lshl_add_u64 v[158:159], v[158:159], 0, s[72:73]
	s_waitcnt lgkmcnt(5)
	v_mfma_f32_32x32x16_f16 v[2:17], v[122:125], v[46:49], v[2:17]
	s_waitcnt lgkmcnt(4)
	v_mfma_f32_32x32x16_f16 v[18:33], v[126:129], v[46:49], v[18:33]
	ds_read_b128 v[122:125], v162 offset:17632
	ds_read_b128 v[126:129], v162 offset:26336
	global_load_dwordx4 v[46:49], v[158:159], off
	v_lshl_add_u64 v[158:159], v[158:159], 0, s[72:73]
	s_waitcnt lgkmcnt(5)
	v_mfma_f32_32x32x16_f16 v[2:17], v[130:133], v[42:45], v[2:17]
	s_waitcnt lgkmcnt(4)
	v_mfma_f32_32x32x16_f16 v[18:33], v[134:137], v[42:45], v[18:33]
	global_load_dwordx4 v[42:45], v[158:159], off
	v_lshl_add_u64 v[158:159], v[158:159], 0, s[72:73]
	s_waitcnt lgkmcnt(3)
	v_mfma_f32_32x32x16_f16 v[2:17], v[114:117], v[38:41], v[2:17]
	s_waitcnt lgkmcnt(2)
	v_mfma_f32_32x32x16_f16 v[18:33], v[118:121], v[38:41], v[18:33]
	global_load_dwordx4 v[38:41], v[158:159], off
	v_lshl_add_u64 v[158:159], v[158:159], 0, s[72:73]
	s_waitcnt lgkmcnt(1)
	v_mfma_f32_32x32x16_f16 v[2:17], v[122:125], v[34:37], v[2:17]
	s_waitcnt lgkmcnt(0)
	v_mfma_f32_32x32x16_f16 v[18:33], v[126:129], v[34:37], v[18:33]
	global_load_dwordx4 v[34:37], v[158:159], off
	v_lshl_add_u64 v[158:159], v[158:159], 0, s[72:73]
	s_waitcnt lgkmcnt(0)
	s_barrier
	ds_read_b128 v[114:117], v162 offset:34816
	ds_read_b128 v[118:121], v162 offset:43520
	ds_read_b128 v[122:125], v162 offset:34848
	ds_read_b128 v[126:129], v162 offset:43552
	ds_read_b128 v[130:133], v162 offset:34880
	ds_read_b128 v[134:137], v162 offset:43584
	s_waitcnt vmcnt(23)
	s_waitcnt lgkmcnt(5)
	v_mfma_f32_32x32x16_f16 v[2:17], v[114:117], v[94:97], v[2:17]
	s_waitcnt lgkmcnt(4)
	v_mfma_f32_32x32x16_f16 v[18:33], v[118:121], v[94:97], v[18:33]
	ds_read_b128 v[114:117], v162 offset:34912
	ds_read_b128 v[118:121], v162 offset:43616
	global_load_dwordx4 v[94:97], v[158:159], off
	v_lshl_add_u64 v[158:159], v[158:159], 0, s[72:73]
	s_waitcnt vmcnt(23)
	s_waitcnt lgkmcnt(5)
	v_mfma_f32_32x32x16_f16 v[2:17], v[122:125], v[98:101], v[2:17]
	s_waitcnt lgkmcnt(4)
	v_mfma_f32_32x32x16_f16 v[18:33], v[126:129], v[98:101], v[18:33]
	ds_read_b128 v[122:125], v162 offset:34944
	ds_read_b128 v[126:129], v162 offset:43648
	global_load_dwordx4 v[98:101], v[158:159], off
	v_lshl_add_u64 v[158:159], v[158:159], 0, s[72:73]
	s_waitcnt vmcnt(23)
	s_waitcnt lgkmcnt(5)
	v_mfma_f32_32x32x16_f16 v[2:17], v[130:133], v[102:105], v[2:17]
	s_waitcnt lgkmcnt(4)
	v_mfma_f32_32x32x16_f16 v[18:33], v[134:137], v[102:105], v[18:33]
	ds_read_b128 v[130:133], v162 offset:34976
	ds_read_b128 v[134:137], v162 offset:43680
	global_load_dwordx4 v[102:105], v[158:159], off
	v_lshl_add_u64 v[158:159], v[158:159], 0, s[72:73]
	s_waitcnt vmcnt(23)
	s_waitcnt lgkmcnt(5)
	v_mfma_f32_32x32x16_f16 v[2:17], v[114:117], v[106:109], v[2:17]
	s_waitcnt lgkmcnt(4)
	v_mfma_f32_32x32x16_f16 v[18:33], v[118:121], v[106:109], v[18:33]
	ds_read_b128 v[114:117], v162 offset:35008
	ds_read_b128 v[118:121], v162 offset:43712
	global_load_dwordx4 v[106:109], v[158:159], off
	v_lshl_add_u64 v[158:159], v[158:159], 0, s[72:73]
	s_waitcnt vmcnt(23)
	s_waitcnt lgkmcnt(5)
	v_mfma_f32_32x32x16_f16 v[2:17], v[122:125], v[142:145], v[2:17]
	s_waitcnt lgkmcnt(4)
	v_mfma_f32_32x32x16_f16 v[18:33], v[126:129], v[142:145], v[18:33]
	ds_read_b128 v[122:125], v162 offset:35040
	ds_read_b128 v[126:129], v162 offset:43744
	global_load_dwordx4 v[142:145], v[158:159], off
	v_lshl_add_u64 v[158:159], v[158:159], 0, s[72:73]
	s_waitcnt vmcnt(23)
	s_waitcnt lgkmcnt(5)
	v_mfma_f32_32x32x16_f16 v[2:17], v[130:133], v[146:149], v[2:17]
	s_waitcnt lgkmcnt(4)
	v_mfma_f32_32x32x16_f16 v[18:33], v[134:137], v[146:149], v[18:33]
	global_load_dwordx4 v[146:149], v[158:159], off
	v_lshl_add_u64 v[158:159], v[158:159], 0, s[72:73]
	s_waitcnt vmcnt(23)
	s_waitcnt lgkmcnt(3)
	v_mfma_f32_32x32x16_f16 v[2:17], v[114:117], v[150:153], v[2:17]
	s_waitcnt lgkmcnt(2)
	v_mfma_f32_32x32x16_f16 v[18:33], v[118:121], v[150:153], v[18:33]
	global_load_dwordx4 v[150:153], v[158:159], off
	v_lshl_add_u64 v[158:159], v[158:159], 0, s[72:73]
	s_waitcnt vmcnt(23)
	s_waitcnt lgkmcnt(1)
	v_mfma_f32_32x32x16_f16 v[2:17], v[122:125], v[154:157], v[2:17]
	s_waitcnt lgkmcnt(0)
	v_mfma_f32_32x32x16_f16 v[18:33], v[126:129], v[154:157], v[18:33]
	global_load_dwordx4 v[154:157], v[158:159], off
	v_lshl_add_u64 v[158:159], v[158:159], 0, s[72:73]
	ds_read_b128 v[114:117], v162 offset:52224
	ds_read_b128 v[118:121], v162 offset:60928
	ds_read_b128 v[122:125], v162 offset:52256
	ds_read_b128 v[126:129], v162 offset:60960
	ds_read_b128 v[130:133], v162 offset:52288
	ds_read_b128 v[134:137], v162 offset:60992
	s_waitcnt vmcnt(23)
	s_waitcnt lgkmcnt(5)
	v_mfma_f32_32x32x16_f16 v[2:17], v[114:117], v[110:113], v[2:17]
	s_waitcnt lgkmcnt(4)
	v_mfma_f32_32x32x16_f16 v[18:33], v[118:121], v[110:113], v[18:33]
	ds_read_b128 v[114:117], v162 offset:52320
	ds_read_b128 v[118:121], v162 offset:61024
	global_load_dwordx4 v[110:113], v[158:159], off
	v_lshl_add_u64 v[158:159], v[158:159], 0, s[72:73]
	s_waitcnt vmcnt(23)
	s_waitcnt lgkmcnt(5)
	v_mfma_f32_32x32x16_f16 v[2:17], v[122:125], v[90:93], v[2:17]
	s_waitcnt lgkmcnt(4)
	v_mfma_f32_32x32x16_f16 v[18:33], v[126:129], v[90:93], v[18:33]
	ds_read_b128 v[122:125], v162 offset:52352
	ds_read_b128 v[126:129], v162 offset:61056
	global_load_dwordx4 v[90:93], v[158:159], off
	v_lshl_add_u64 v[158:159], v[158:159], 0, s[72:73]
	s_waitcnt vmcnt(23)
	s_waitcnt lgkmcnt(5)
	v_mfma_f32_32x32x16_f16 v[2:17], v[130:133], v[86:89], v[2:17]
	s_waitcnt lgkmcnt(4)
	v_mfma_f32_32x32x16_f16 v[18:33], v[134:137], v[86:89], v[18:33]
	ds_read_b128 v[130:133], v162 offset:52384
	ds_read_b128 v[134:137], v162 offset:61088
	global_load_dwordx4 v[86:89], v[158:159], off
	v_lshl_add_u64 v[158:159], v[158:159], 0, s[72:73]
	s_waitcnt vmcnt(23)
	s_waitcnt lgkmcnt(5)
	v_mfma_f32_32x32x16_f16 v[2:17], v[114:117], v[82:85], v[2:17]
	s_waitcnt lgkmcnt(4)
	v_mfma_f32_32x32x16_f16 v[18:33], v[118:121], v[82:85], v[18:33]
	ds_read_b128 v[114:117], v162 offset:52416
	ds_read_b128 v[118:121], v162 offset:61120
	global_load_dwordx4 v[82:85], v[158:159], off
	v_lshl_add_u64 v[158:159], v[158:159], 0, s[72:73]
	s_waitcnt vmcnt(23)
	s_waitcnt lgkmcnt(5)
	v_mfma_f32_32x32x16_f16 v[2:17], v[122:125], v[78:81], v[2:17]
	s_waitcnt lgkmcnt(4)
	v_mfma_f32_32x32x16_f16 v[18:33], v[126:129], v[78:81], v[18:33]
	ds_read_b128 v[122:125], v162 offset:52448
	ds_read_b128 v[126:129], v162 offset:61152
	global_load_dwordx4 v[78:81], v[158:159], off
	v_lshl_add_u64 v[158:159], v[158:159], 0, s[72:73]
	s_waitcnt vmcnt(23)
	s_waitcnt lgkmcnt(5)
	v_mfma_f32_32x32x16_f16 v[2:17], v[130:133], v[74:77], v[2:17]
	s_waitcnt lgkmcnt(4)
	v_mfma_f32_32x32x16_f16 v[18:33], v[134:137], v[74:77], v[18:33]
	global_load_dwordx4 v[74:77], v[158:159], off
	v_lshl_add_u64 v[158:159], v[158:159], 0, s[72:73]
	s_waitcnt vmcnt(23)
	s_waitcnt lgkmcnt(3)
	v_mfma_f32_32x32x16_f16 v[2:17], v[114:117], v[70:73], v[2:17]
	s_waitcnt lgkmcnt(2)
	v_mfma_f32_32x32x16_f16 v[18:33], v[118:121], v[70:73], v[18:33]
	global_load_dwordx4 v[70:73], v[158:159], off
	v_lshl_add_u64 v[158:159], v[158:159], 0, s[72:73]
	s_waitcnt vmcnt(23)
	s_waitcnt lgkmcnt(1)
	v_mfma_f32_32x32x16_f16 v[2:17], v[122:125], v[66:69], v[2:17]
	s_waitcnt lgkmcnt(0)
	v_mfma_f32_32x32x16_f16 v[18:33], v[126:129], v[66:69], v[18:33]
	global_load_dwordx4 v[66:69], v[158:159], off
	v_lshl_add_u64 v[158:159], v[158:159], 0, s[72:73]
	s_waitcnt lgkmcnt(0)
	s_barrier
	ds_read_b128 v[114:117], v163 offset:0
	ds_read_b128 v[118:121], v163 offset:8704
	ds_read_b128 v[122:125], v163 offset:32
	ds_read_b128 v[126:129], v163 offset:8736
	ds_read_b128 v[130:133], v163 offset:64
	ds_read_b128 v[134:137], v163 offset:8768
	s_waitcnt vmcnt(23)
	s_waitcnt lgkmcnt(5)
	v_mfma_f32_32x32x16_f16 v[2:17], v[114:117], v[62:65], v[2:17]
	s_waitcnt lgkmcnt(4)
	v_mfma_f32_32x32x16_f16 v[18:33], v[118:121], v[62:65], v[18:33]
	ds_read_b128 v[114:117], v163 offset:96
	ds_read_b128 v[118:121], v163 offset:8800
	global_load_dwordx4 v[62:65], v[158:159], off
	v_lshl_add_u64 v[158:159], v[158:159], 0, s[72:73]
	s_waitcnt vmcnt(23)
	s_waitcnt lgkmcnt(5)
	v_mfma_f32_32x32x16_f16 v[2:17], v[122:125], v[58:61], v[2:17]
	s_waitcnt lgkmcnt(4)
	v_mfma_f32_32x32x16_f16 v[18:33], v[126:129], v[58:61], v[18:33]
	ds_read_b128 v[122:125], v163 offset:128
	ds_read_b128 v[126:129], v163 offset:8832
	global_load_dwordx4 v[58:61], v[158:159], off
	v_lshl_add_u64 v[158:159], v[158:159], 0, s[72:73]
	s_waitcnt vmcnt(23)
	s_waitcnt lgkmcnt(5)
	v_mfma_f32_32x32x16_f16 v[2:17], v[130:133], v[54:57], v[2:17]
	s_waitcnt lgkmcnt(4)
	v_mfma_f32_32x32x16_f16 v[18:33], v[134:137], v[54:57], v[18:33]
	ds_read_b128 v[130:133], v163 offset:160
	ds_read_b128 v[134:137], v163 offset:8864
	global_load_dwordx4 v[54:57], v[158:159], off
	v_lshl_add_u64 v[158:159], v[158:159], 0, s[72:73]
	s_waitcnt vmcnt(23)
	s_waitcnt lgkmcnt(5)
	v_mfma_f32_32x32x16_f16 v[2:17], v[114:117], v[50:53], v[2:17]
	s_waitcnt lgkmcnt(4)
	v_mfma_f32_32x32x16_f16 v[18:33], v[118:121], v[50:53], v[18:33]
	ds_read_b128 v[114:117], v163 offset:192
	ds_read_b128 v[118:121], v163 offset:8896
	global_load_dwordx4 v[50:53], v[158:159], off
	v_lshl_add_u64 v[158:159], v[158:159], 0, s[72:73]
	s_waitcnt vmcnt(23)
	s_waitcnt lgkmcnt(5)
	v_mfma_f32_32x32x16_f16 v[2:17], v[122:125], v[46:49], v[2:17]
	s_waitcnt lgkmcnt(4)
	v_mfma_f32_32x32x16_f16 v[18:33], v[126:129], v[46:49], v[18:33]
	ds_read_b128 v[122:125], v163 offset:224
	ds_read_b128 v[126:129], v163 offset:8928
	global_load_dwordx4 v[46:49], v[158:159], off
	v_lshl_add_u64 v[158:159], v[158:159], 0, s[72:73]
	s_waitcnt vmcnt(23)
	s_waitcnt lgkmcnt(5)
	v_mfma_f32_32x32x16_f16 v[2:17], v[130:133], v[42:45], v[2:17]
	s_waitcnt lgkmcnt(4)
	v_mfma_f32_32x32x16_f16 v[18:33], v[134:137], v[42:45], v[18:33]
	global_load_dwordx4 v[42:45], v[158:159], off
	v_lshl_add_u64 v[158:159], v[158:159], 0, s[72:73]
	s_waitcnt vmcnt(23)
	s_waitcnt lgkmcnt(3)
	v_mfma_f32_32x32x16_f16 v[2:17], v[114:117], v[38:41], v[2:17]
	s_waitcnt lgkmcnt(2)
	v_mfma_f32_32x32x16_f16 v[18:33], v[118:121], v[38:41], v[18:33]
	global_load_dwordx4 v[38:41], v[158:159], off
	v_lshl_add_u64 v[158:159], v[158:159], 0, s[72:73]
	s_waitcnt vmcnt(23)
	s_waitcnt lgkmcnt(1)
	v_mfma_f32_32x32x16_f16 v[2:17], v[122:125], v[34:37], v[2:17]
	s_waitcnt lgkmcnt(0)
	v_mfma_f32_32x32x16_f16 v[18:33], v[126:129], v[34:37], v[18:33]
	global_load_dwordx4 v[34:37], v[158:159], off
	v_lshl_add_u64 v[158:159], v[158:159], 0, s[72:73]
	ds_read_b128 v[114:117], v162 offset:0
	ds_read_b128 v[118:121], v162 offset:8704
	ds_read_b128 v[122:125], v162 offset:32
	ds_read_b128 v[126:129], v162 offset:8736
	ds_read_b128 v[130:133], v162 offset:64
	ds_read_b128 v[134:137], v162 offset:8768
	s_waitcnt vmcnt(23)
	s_waitcnt lgkmcnt(5)
	v_mfma_f32_32x32x16_f16 v[2:17], v[114:117], v[94:97], v[2:17]
	s_waitcnt lgkmcnt(4)
	v_mfma_f32_32x32x16_f16 v[18:33], v[118:121], v[94:97], v[18:33]
	ds_read_b128 v[114:117], v162 offset:96
	ds_read_b128 v[118:121], v162 offset:8800
	global_load_dwordx4 v[94:97], v[158:159], off
	v_lshl_add_u64 v[158:159], v[158:159], 0, s[72:73]
	s_waitcnt vmcnt(23)
	s_waitcnt lgkmcnt(5)
	v_mfma_f32_32x32x16_f16 v[2:17], v[122:125], v[98:101], v[2:17]
	s_waitcnt lgkmcnt(4)
	v_mfma_f32_32x32x16_f16 v[18:33], v[126:129], v[98:101], v[18:33]
	ds_read_b128 v[122:125], v162 offset:128
	ds_read_b128 v[126:129], v162 offset:8832
	global_load_dwordx4 v[98:101], v[158:159], off
	v_lshl_add_u64 v[158:159], v[158:159], 0, s[72:73]
	s_waitcnt vmcnt(23)
	s_waitcnt lgkmcnt(5)
	v_mfma_f32_32x32x16_f16 v[2:17], v[130:133], v[102:105], v[2:17]
	s_waitcnt lgkmcnt(4)
	v_mfma_f32_32x32x16_f16 v[18:33], v[134:137], v[102:105], v[18:33]
	ds_read_b128 v[130:133], v162 offset:160
	ds_read_b128 v[134:137], v162 offset:8864
	global_load_dwordx4 v[102:105], v[158:159], off
	v_lshl_add_u64 v[158:159], v[158:159], 0, s[72:73]
	s_waitcnt vmcnt(23)
	s_waitcnt lgkmcnt(5)
	v_mfma_f32_32x32x16_f16 v[2:17], v[114:117], v[106:109], v[2:17]
	s_waitcnt lgkmcnt(4)
	v_mfma_f32_32x32x16_f16 v[18:33], v[118:121], v[106:109], v[18:33]
	ds_read_b128 v[114:117], v162 offset:192
	ds_read_b128 v[118:121], v162 offset:8896
	global_load_dwordx4 v[106:109], v[158:159], off
	v_lshl_add_u64 v[158:159], v[158:159], 0, s[72:73]
	s_waitcnt vmcnt(23)
	s_waitcnt lgkmcnt(5)
	v_mfma_f32_32x32x16_f16 v[2:17], v[122:125], v[142:145], v[2:17]
	s_waitcnt lgkmcnt(4)
	v_mfma_f32_32x32x16_f16 v[18:33], v[126:129], v[142:145], v[18:33]
	ds_read_b128 v[122:125], v162 offset:224
	ds_read_b128 v[126:129], v162 offset:8928
	global_load_dwordx4 v[142:145], v[158:159], off
	v_lshl_add_u64 v[158:159], v[158:159], 0, s[72:73]
	s_waitcnt vmcnt(23)
	s_waitcnt lgkmcnt(5)
	v_mfma_f32_32x32x16_f16 v[2:17], v[130:133], v[146:149], v[2:17]
	s_waitcnt lgkmcnt(4)
	v_mfma_f32_32x32x16_f16 v[18:33], v[134:137], v[146:149], v[18:33]
	global_load_dwordx4 v[146:149], v[158:159], off
	v_lshl_add_u64 v[158:159], v[158:159], 0, s[72:73]
	s_waitcnt vmcnt(23)
	s_waitcnt lgkmcnt(3)
	v_mfma_f32_32x32x16_f16 v[2:17], v[114:117], v[150:153], v[2:17]
	s_waitcnt lgkmcnt(2)
	v_mfma_f32_32x32x16_f16 v[18:33], v[118:121], v[150:153], v[18:33]
	global_load_dwordx4 v[150:153], v[158:159], off
	v_lshl_add_u64 v[158:159], v[158:159], 0, s[72:73]
	s_waitcnt vmcnt(23)
	s_waitcnt lgkmcnt(1)
	v_mfma_f32_32x32x16_f16 v[2:17], v[122:125], v[154:157], v[2:17]
	s_waitcnt lgkmcnt(0)
	v_mfma_f32_32x32x16_f16 v[18:33], v[126:129], v[154:157], v[18:33]
	global_load_dwordx4 v[154:157], v[158:159], off
	v_lshl_add_u64 v[158:159], v[158:159], 0, s[72:73]
	s_waitcnt lgkmcnt(0)
	s_barrier
	ds_read_b128 v[114:117], v162 offset:17408
	ds_read_b128 v[118:121], v162 offset:26112
	ds_read_b128 v[122:125], v162 offset:17440
	ds_read_b128 v[126:129], v162 offset:26144
	ds_read_b128 v[130:133], v162 offset:17472
	ds_read_b128 v[134:137], v162 offset:26176
	s_waitcnt vmcnt(23)
	s_waitcnt lgkmcnt(5)
	v_mfma_f32_32x32x16_f16 v[2:17], v[114:117], v[110:113], v[2:17]
	s_waitcnt lgkmcnt(4)
	v_mfma_f32_32x32x16_f16 v[18:33], v[118:121], v[110:113], v[18:33]
	ds_read_b128 v[114:117], v162 offset:17504
	ds_read_b128 v[118:121], v162 offset:26208
	global_load_dwordx4 v[110:113], v[158:159], off
	v_lshl_add_u64 v[158:159], v[158:159], 0, s[72:73]
	s_waitcnt vmcnt(23)
	s_waitcnt lgkmcnt(5)
	v_mfma_f32_32x32x16_f16 v[2:17], v[122:125], v[90:93], v[2:17]
	s_waitcnt lgkmcnt(4)
	v_mfma_f32_32x32x16_f16 v[18:33], v[126:129], v[90:93], v[18:33]
	ds_read_b128 v[122:125], v162 offset:17536
	ds_read_b128 v[126:129], v162 offset:26240
	global_load_dwordx4 v[90:93], v[158:159], off
	v_lshl_add_u64 v[158:159], v[158:159], 0, s[72:73]
	s_waitcnt vmcnt(23)
	s_waitcnt lgkmcnt(5)
	v_mfma_f32_32x32x16_f16 v[2:17], v[130:133], v[86:89], v[2:17]
	s_waitcnt lgkmcnt(4)
	v_mfma_f32_32x32x16_f16 v[18:33], v[134:137], v[86:89], v[18:33]
	ds_read_b128 v[130:133], v162 offset:17568
	ds_read_b128 v[134:137], v162 offset:26272
	global_load_dwordx4 v[86:89], v[158:159], off
	v_lshl_add_u64 v[158:159], v[158:159], 0, s[72:73]
	s_waitcnt vmcnt(23)
	s_waitcnt lgkmcnt(5)
	v_mfma_f32_32x32x16_f16 v[2:17], v[114:117], v[82:85], v[2:17]
	s_waitcnt lgkmcnt(4)
	v_mfma_f32_32x32x16_f16 v[18:33], v[118:121], v[82:85], v[18:33]
	ds_read_b128 v[114:117], v162 offset:17600
	ds_read_b128 v[118:121], v162 offset:26304
	global_load_dwordx4 v[82:85], v[158:159], off
	v_lshl_add_u64 v[158:159], v[158:159], 0, s[72:73]
	s_waitcnt vmcnt(23)
	s_waitcnt lgkmcnt(5)
	v_mfma_f32_32x32x16_f16 v[2:17], v[122:125], v[78:81], v[2:17]
	s_waitcnt lgkmcnt(4)
	v_mfma_f32_32x32x16_f16 v[18:33], v[126:129], v[78:81], v[18:33]
	ds_read_b128 v[122:125], v162 offset:17632
	ds_read_b128 v[126:129], v162 offset:26336
	global_load_dwordx4 v[78:81], v[158:159], off
	v_lshl_add_u64 v[158:159], v[158:159], 0, s[72:73]
	s_waitcnt vmcnt(23)
	s_waitcnt lgkmcnt(5)
	v_mfma_f32_32x32x16_f16 v[2:17], v[130:133], v[74:77], v[2:17]
	s_waitcnt lgkmcnt(4)
	v_mfma_f32_32x32x16_f16 v[18:33], v[134:137], v[74:77], v[18:33]
	global_load_dwordx4 v[74:77], v[158:159], off
	v_lshl_add_u64 v[158:159], v[158:159], 0, s[72:73]
	s_waitcnt vmcnt(23)
	s_waitcnt lgkmcnt(3)
	v_mfma_f32_32x32x16_f16 v[2:17], v[114:117], v[70:73], v[2:17]
	s_waitcnt lgkmcnt(2)
	v_mfma_f32_32x32x16_f16 v[18:33], v[118:121], v[70:73], v[18:33]
	global_load_dwordx4 v[70:73], v[158:159], off
	v_lshl_add_u64 v[158:159], v[158:159], 0, s[72:73]
	s_waitcnt vmcnt(23)
	s_waitcnt lgkmcnt(1)
	v_mfma_f32_32x32x16_f16 v[2:17], v[122:125], v[66:69], v[2:17]
	s_waitcnt lgkmcnt(0)
	v_mfma_f32_32x32x16_f16 v[18:33], v[126:129], v[66:69], v[18:33]
	global_load_dwordx4 v[66:69], v[158:159], off
	v_lshl_add_u64 v[158:159], v[158:159], 0, s[72:73]
	ds_read_b128 v[114:117], v162 offset:34816
	ds_read_b128 v[118:121], v162 offset:43520
	ds_read_b128 v[122:125], v162 offset:34848
	ds_read_b128 v[126:129], v162 offset:43552
	ds_read_b128 v[130:133], v162 offset:34880
	ds_read_b128 v[134:137], v162 offset:43584
	s_waitcnt vmcnt(23)
	s_waitcnt lgkmcnt(5)
	v_mfma_f32_32x32x16_f16 v[2:17], v[114:117], v[62:65], v[2:17]
	s_waitcnt lgkmcnt(4)
	v_mfma_f32_32x32x16_f16 v[18:33], v[118:121], v[62:65], v[18:33]
	ds_read_b128 v[114:117], v162 offset:34912
	ds_read_b128 v[118:121], v162 offset:43616
	global_load_dwordx4 v[62:65], v[158:159], off
	v_lshl_add_u64 v[158:159], v[158:159], 0, s[72:73]
	s_waitcnt vmcnt(23)
	s_waitcnt lgkmcnt(5)
	v_mfma_f32_32x32x16_f16 v[2:17], v[122:125], v[58:61], v[2:17]
	s_waitcnt lgkmcnt(4)
	v_mfma_f32_32x32x16_f16 v[18:33], v[126:129], v[58:61], v[18:33]
	ds_read_b128 v[122:125], v162 offset:34944
	ds_read_b128 v[126:129], v162 offset:43648
	global_load_dwordx4 v[58:61], v[158:159], off
	v_lshl_add_u64 v[158:159], v[158:159], 0, s[72:73]
	s_waitcnt vmcnt(23)
	s_waitcnt lgkmcnt(5)
	v_mfma_f32_32x32x16_f16 v[2:17], v[130:133], v[54:57], v[2:17]
	s_waitcnt lgkmcnt(4)
	v_mfma_f32_32x32x16_f16 v[18:33], v[134:137], v[54:57], v[18:33]
	ds_read_b128 v[130:133], v162 offset:34976
	ds_read_b128 v[134:137], v162 offset:43680
	global_load_dwordx4 v[54:57], v[158:159], off
	v_lshl_add_u64 v[158:159], v[158:159], 0, s[72:73]
	s_waitcnt vmcnt(23)
	s_waitcnt lgkmcnt(5)
	v_mfma_f32_32x32x16_f16 v[2:17], v[114:117], v[50:53], v[2:17]
	s_waitcnt lgkmcnt(4)
	v_mfma_f32_32x32x16_f16 v[18:33], v[118:121], v[50:53], v[18:33]
	ds_read_b128 v[114:117], v162 offset:35008
	ds_read_b128 v[118:121], v162 offset:43712
	global_load_dwordx4 v[50:53], v[158:159], off
	v_lshl_add_u64 v[158:159], v[158:159], 0, s[72:73]
	s_waitcnt vmcnt(23)
	s_waitcnt lgkmcnt(5)
	v_mfma_f32_32x32x16_f16 v[2:17], v[122:125], v[46:49], v[2:17]
	s_waitcnt lgkmcnt(4)
	v_mfma_f32_32x32x16_f16 v[18:33], v[126:129], v[46:49], v[18:33]
	ds_read_b128 v[122:125], v162 offset:35040
	ds_read_b128 v[126:129], v162 offset:43744
	global_load_dwordx4 v[46:49], v[158:159], off
	v_lshl_add_u64 v[158:159], v[158:159], 0, s[72:73]
	s_waitcnt vmcnt(23)
	s_waitcnt lgkmcnt(5)
	v_mfma_f32_32x32x16_f16 v[2:17], v[130:133], v[42:45], v[2:17]
	s_waitcnt lgkmcnt(4)
	v_mfma_f32_32x32x16_f16 v[18:33], v[134:137], v[42:45], v[18:33]
	global_load_dwordx4 v[42:45], v[158:159], off
	v_lshl_add_u64 v[158:159], v[158:159], 0, s[72:73]
	s_waitcnt vmcnt(23)
	s_waitcnt lgkmcnt(3)
	v_mfma_f32_32x32x16_f16 v[2:17], v[114:117], v[38:41], v[2:17]
	s_waitcnt lgkmcnt(2)
	v_mfma_f32_32x32x16_f16 v[18:33], v[118:121], v[38:41], v[18:33]
	global_load_dwordx4 v[38:41], v[158:159], off
	v_lshl_add_u64 v[158:159], v[158:159], 0, s[72:73]
	s_waitcnt vmcnt(23)
	s_waitcnt lgkmcnt(1)
	v_mfma_f32_32x32x16_f16 v[2:17], v[122:125], v[34:37], v[2:17]
	s_waitcnt lgkmcnt(0)
	v_mfma_f32_32x32x16_f16 v[18:33], v[126:129], v[34:37], v[18:33]
	global_load_dwordx4 v[34:37], v[158:159], off
	v_lshl_add_u64 v[158:159], v[158:159], 0, s[72:73]
	s_waitcnt lgkmcnt(0)
	s_barrier
	ds_read_b128 v[114:117], v162 offset:52224
	ds_read_b128 v[118:121], v162 offset:60928
	ds_read_b128 v[122:125], v162 offset:52256
	ds_read_b128 v[126:129], v162 offset:60960
	ds_read_b128 v[130:133], v162 offset:52288
	ds_read_b128 v[134:137], v162 offset:60992
	s_waitcnt vmcnt(23)
	s_waitcnt lgkmcnt(5)
	v_mfma_f32_32x32x16_f16 v[2:17], v[114:117], v[94:97], v[2:17]
	s_waitcnt lgkmcnt(4)
	v_mfma_f32_32x32x16_f16 v[18:33], v[118:121], v[94:97], v[18:33]
	ds_read_b128 v[114:117], v162 offset:52320
	ds_read_b128 v[118:121], v162 offset:61024
	global_load_dwordx4 v[94:97], v[158:159], off
	v_lshl_add_u64 v[158:159], v[158:159], 0, s[72:73]
	s_waitcnt vmcnt(23)
	s_waitcnt lgkmcnt(5)
	v_mfma_f32_32x32x16_f16 v[2:17], v[122:125], v[98:101], v[2:17]
	s_waitcnt lgkmcnt(4)
	v_mfma_f32_32x32x16_f16 v[18:33], v[126:129], v[98:101], v[18:33]
	ds_read_b128 v[122:125], v162 offset:52352
	ds_read_b128 v[126:129], v162 offset:61056
	global_load_dwordx4 v[98:101], v[158:159], off
	v_lshl_add_u64 v[158:159], v[158:159], 0, s[72:73]
	s_waitcnt vmcnt(23)
	s_waitcnt lgkmcnt(5)
	v_mfma_f32_32x32x16_f16 v[2:17], v[130:133], v[102:105], v[2:17]
	s_waitcnt lgkmcnt(4)
	v_mfma_f32_32x32x16_f16 v[18:33], v[134:137], v[102:105], v[18:33]
	ds_read_b128 v[130:133], v162 offset:52384
	ds_read_b128 v[134:137], v162 offset:61088
	global_load_dwordx4 v[102:105], v[158:159], off
	v_lshl_add_u64 v[158:159], v[158:159], 0, s[72:73]
	s_waitcnt vmcnt(23)
	s_waitcnt lgkmcnt(5)
	v_mfma_f32_32x32x16_f16 v[2:17], v[114:117], v[106:109], v[2:17]
	s_waitcnt lgkmcnt(4)
	v_mfma_f32_32x32x16_f16 v[18:33], v[118:121], v[106:109], v[18:33]
	ds_read_b128 v[114:117], v162 offset:52416
	ds_read_b128 v[118:121], v162 offset:61120
	global_load_dwordx4 v[106:109], v[158:159], off
	v_lshl_add_u64 v[158:159], v[158:159], 0, s[72:73]
	s_waitcnt vmcnt(23)
	s_waitcnt lgkmcnt(5)
	v_mfma_f32_32x32x16_f16 v[2:17], v[122:125], v[142:145], v[2:17]
	s_waitcnt lgkmcnt(4)
	v_mfma_f32_32x32x16_f16 v[18:33], v[126:129], v[142:145], v[18:33]
	ds_read_b128 v[122:125], v162 offset:52448
	ds_read_b128 v[126:129], v162 offset:61152
	global_load_dwordx4 v[142:145], v[158:159], off
	v_lshl_add_u64 v[158:159], v[158:159], 0, s[72:73]
	s_waitcnt vmcnt(23)
	s_waitcnt lgkmcnt(5)
	v_mfma_f32_32x32x16_f16 v[2:17], v[130:133], v[146:149], v[2:17]
	s_waitcnt lgkmcnt(4)
	v_mfma_f32_32x32x16_f16 v[18:33], v[134:137], v[146:149], v[18:33]
	global_load_dwordx4 v[146:149], v[158:159], off
	v_lshl_add_u64 v[158:159], v[158:159], 0, s[72:73]
	s_waitcnt vmcnt(23)
	s_waitcnt lgkmcnt(3)
	v_mfma_f32_32x32x16_f16 v[2:17], v[114:117], v[150:153], v[2:17]
	s_waitcnt lgkmcnt(2)
	v_mfma_f32_32x32x16_f16 v[18:33], v[118:121], v[150:153], v[18:33]
	global_load_dwordx4 v[150:153], v[158:159], off
	v_lshl_add_u64 v[158:159], v[158:159], 0, s[72:73]
	s_waitcnt vmcnt(23)
	s_waitcnt lgkmcnt(1)
	v_mfma_f32_32x32x16_f16 v[2:17], v[122:125], v[154:157], v[2:17]
	s_waitcnt lgkmcnt(0)
	v_mfma_f32_32x32x16_f16 v[18:33], v[126:129], v[154:157], v[18:33]
	global_load_dwordx4 v[154:157], v[158:159], off
	v_lshl_add_u64 v[158:159], v[158:159], 0, s[72:73]
	ds_read_b128 v[114:117], v163 offset:0
	ds_read_b128 v[118:121], v163 offset:8704
	ds_read_b128 v[122:125], v163 offset:32
	ds_read_b128 v[126:129], v163 offset:8736
	ds_read_b128 v[130:133], v163 offset:64
	ds_read_b128 v[134:137], v163 offset:8768
	s_waitcnt vmcnt(23)
	s_waitcnt lgkmcnt(5)
	v_mfma_f32_32x32x16_f16 v[2:17], v[114:117], v[110:113], v[2:17]
	s_waitcnt lgkmcnt(4)
	v_mfma_f32_32x32x16_f16 v[18:33], v[118:121], v[110:113], v[18:33]
	ds_read_b128 v[114:117], v163 offset:96
	ds_read_b128 v[118:121], v163 offset:8800
	global_load_dwordx4 v[110:113], v[158:159], off
	v_lshl_add_u64 v[158:159], v[158:159], 0, s[72:73]
	s_waitcnt vmcnt(23)
	s_waitcnt lgkmcnt(5)
	v_mfma_f32_32x32x16_f16 v[2:17], v[122:125], v[90:93], v[2:17]
	s_waitcnt lgkmcnt(4)
	v_mfma_f32_32x32x16_f16 v[18:33], v[126:129], v[90:93], v[18:33]
	ds_read_b128 v[122:125], v163 offset:128
	ds_read_b128 v[126:129], v163 offset:8832
	global_load_dwordx4 v[90:93], v[158:159], off
	v_lshl_add_u64 v[158:159], v[158:159], 0, s[72:73]
	s_waitcnt vmcnt(23)
	s_waitcnt lgkmcnt(5)
	v_mfma_f32_32x32x16_f16 v[2:17], v[130:133], v[86:89], v[2:17]
	s_waitcnt lgkmcnt(4)
	v_mfma_f32_32x32x16_f16 v[18:33], v[134:137], v[86:89], v[18:33]
	ds_read_b128 v[130:133], v163 offset:160
	ds_read_b128 v[134:137], v163 offset:8864
	global_load_dwordx4 v[86:89], v[158:159], off
	v_lshl_add_u64 v[158:159], v[158:159], 0, s[72:73]
	s_waitcnt vmcnt(23)
	s_waitcnt lgkmcnt(5)
	v_mfma_f32_32x32x16_f16 v[2:17], v[114:117], v[82:85], v[2:17]
	s_waitcnt lgkmcnt(4)
	v_mfma_f32_32x32x16_f16 v[18:33], v[118:121], v[82:85], v[18:33]
	ds_read_b128 v[114:117], v163 offset:192
	ds_read_b128 v[118:121], v163 offset:8896
	global_load_dwordx4 v[82:85], v[158:159], off
	v_lshl_add_u64 v[158:159], v[158:159], 0, s[72:73]
	s_waitcnt vmcnt(23)
	s_waitcnt lgkmcnt(5)
	v_mfma_f32_32x32x16_f16 v[2:17], v[122:125], v[78:81], v[2:17]
	s_waitcnt lgkmcnt(4)
	v_mfma_f32_32x32x16_f16 v[18:33], v[126:129], v[78:81], v[18:33]
	ds_read_b128 v[122:125], v163 offset:224
	ds_read_b128 v[126:129], v163 offset:8928
	global_load_dwordx4 v[78:81], v[158:159], off
	v_lshl_add_u64 v[158:159], v[158:159], 0, s[72:73]
	s_waitcnt vmcnt(23)
	s_waitcnt lgkmcnt(5)
	v_mfma_f32_32x32x16_f16 v[2:17], v[130:133], v[74:77], v[2:17]
	s_waitcnt lgkmcnt(4)
	v_mfma_f32_32x32x16_f16 v[18:33], v[134:137], v[74:77], v[18:33]
	global_load_dwordx4 v[74:77], v[158:159], off
	v_lshl_add_u64 v[158:159], v[158:159], 0, s[72:73]
	s_waitcnt vmcnt(23)
	s_waitcnt lgkmcnt(3)
	v_mfma_f32_32x32x16_f16 v[2:17], v[114:117], v[70:73], v[2:17]
	s_waitcnt lgkmcnt(2)
	v_mfma_f32_32x32x16_f16 v[18:33], v[118:121], v[70:73], v[18:33]
	global_load_dwordx4 v[70:73], v[158:159], off
	v_lshl_add_u64 v[158:159], v[158:159], 0, s[72:73]
	s_waitcnt vmcnt(23)
	s_waitcnt lgkmcnt(1)
	v_mfma_f32_32x32x16_f16 v[2:17], v[122:125], v[66:69], v[2:17]
	s_waitcnt lgkmcnt(0)
	v_mfma_f32_32x32x16_f16 v[18:33], v[126:129], v[66:69], v[18:33]
	global_load_dwordx4 v[66:69], v[158:159], off
	v_lshl_add_u64 v[158:159], v[158:159], 0, s[72:73]
	s_waitcnt lgkmcnt(0)
	s_barrier
	ds_read_b128 v[114:117], v162 offset:0
	ds_read_b128 v[118:121], v162 offset:8704
	ds_read_b128 v[122:125], v162 offset:32
	ds_read_b128 v[126:129], v162 offset:8736
	ds_read_b128 v[130:133], v162 offset:64
	ds_read_b128 v[134:137], v162 offset:8768
	s_waitcnt vmcnt(23)
	s_waitcnt lgkmcnt(5)
	v_mfma_f32_32x32x16_f16 v[2:17], v[114:117], v[62:65], v[2:17]
	s_waitcnt lgkmcnt(4)
	v_mfma_f32_32x32x16_f16 v[18:33], v[118:121], v[62:65], v[18:33]
	ds_read_b128 v[114:117], v162 offset:96
	ds_read_b128 v[118:121], v162 offset:8800
	global_load_dwordx4 v[62:65], v[158:159], off
	v_lshl_add_u64 v[158:159], v[158:159], 0, s[72:73]
	s_waitcnt vmcnt(23)
	s_waitcnt lgkmcnt(5)
	v_mfma_f32_32x32x16_f16 v[2:17], v[122:125], v[58:61], v[2:17]
	s_waitcnt lgkmcnt(4)
	v_mfma_f32_32x32x16_f16 v[18:33], v[126:129], v[58:61], v[18:33]
	ds_read_b128 v[122:125], v162 offset:128
	ds_read_b128 v[126:129], v162 offset:8832
	global_load_dwordx4 v[58:61], v[158:159], off
	v_lshl_add_u64 v[158:159], v[158:159], 0, s[72:73]
	s_waitcnt vmcnt(23)
	s_waitcnt lgkmcnt(5)
	v_mfma_f32_32x32x16_f16 v[2:17], v[130:133], v[54:57], v[2:17]
	s_waitcnt lgkmcnt(4)
	v_mfma_f32_32x32x16_f16 v[18:33], v[134:137], v[54:57], v[18:33]
	ds_read_b128 v[130:133], v162 offset:160
	ds_read_b128 v[134:137], v162 offset:8864
	global_load_dwordx4 v[54:57], v[158:159], off
	v_lshl_add_u64 v[158:159], v[158:159], 0, s[72:73]
	s_waitcnt vmcnt(23)
	s_waitcnt lgkmcnt(5)
	v_mfma_f32_32x32x16_f16 v[2:17], v[114:117], v[50:53], v[2:17]
	s_waitcnt lgkmcnt(4)
	v_mfma_f32_32x32x16_f16 v[18:33], v[118:121], v[50:53], v[18:33]
	ds_read_b128 v[114:117], v162 offset:192
	ds_read_b128 v[118:121], v162 offset:8896
	global_load_dwordx4 v[50:53], v[158:159], off
	v_lshl_add_u64 v[158:159], v[158:159], 0, s[72:73]
	s_waitcnt vmcnt(23)
	s_waitcnt lgkmcnt(5)
	v_mfma_f32_32x32x16_f16 v[2:17], v[122:125], v[46:49], v[2:17]
	s_waitcnt lgkmcnt(4)
	v_mfma_f32_32x32x16_f16 v[18:33], v[126:129], v[46:49], v[18:33]
	ds_read_b128 v[122:125], v162 offset:224
	ds_read_b128 v[126:129], v162 offset:8928
	global_load_dwordx4 v[46:49], v[158:159], off
	v_lshl_add_u64 v[158:159], v[158:159], 0, s[72:73]
	s_waitcnt vmcnt(23)
	s_waitcnt lgkmcnt(5)
	v_mfma_f32_32x32x16_f16 v[2:17], v[130:133], v[42:45], v[2:17]
	s_waitcnt lgkmcnt(4)
	v_mfma_f32_32x32x16_f16 v[18:33], v[134:137], v[42:45], v[18:33]
	global_load_dwordx4 v[42:45], v[158:159], off
	v_lshl_add_u64 v[158:159], v[158:159], 0, s[72:73]
	s_waitcnt vmcnt(23)
	s_waitcnt lgkmcnt(3)
	v_mfma_f32_32x32x16_f16 v[2:17], v[114:117], v[38:41], v[2:17]
	s_waitcnt lgkmcnt(2)
	v_mfma_f32_32x32x16_f16 v[18:33], v[118:121], v[38:41], v[18:33]
	global_load_dwordx4 v[38:41], v[158:159], off
	v_lshl_add_u64 v[158:159], v[158:159], 0, s[72:73]
	s_waitcnt vmcnt(23)
	s_waitcnt lgkmcnt(1)
	v_mfma_f32_32x32x16_f16 v[2:17], v[122:125], v[34:37], v[2:17]
	s_waitcnt lgkmcnt(0)
	v_mfma_f32_32x32x16_f16 v[18:33], v[126:129], v[34:37], v[18:33]
	global_load_dwordx4 v[34:37], v[158:159], off
	v_lshl_add_u64 v[158:159], v[158:159], 0, s[72:73]
	ds_read_b128 v[114:117], v162 offset:17408
	ds_read_b128 v[118:121], v162 offset:26112
	ds_read_b128 v[122:125], v162 offset:17440
	ds_read_b128 v[126:129], v162 offset:26144
	ds_read_b128 v[130:133], v162 offset:17472
	ds_read_b128 v[134:137], v162 offset:26176
	s_waitcnt vmcnt(23)
	s_waitcnt lgkmcnt(5)
	v_mfma_f32_32x32x16_f16 v[2:17], v[114:117], v[94:97], v[2:17]
	s_waitcnt lgkmcnt(4)
	v_mfma_f32_32x32x16_f16 v[18:33], v[118:121], v[94:97], v[18:33]
	ds_read_b128 v[114:117], v162 offset:17504
	ds_read_b128 v[118:121], v162 offset:26208
	global_load_dwordx4 v[94:97], v[158:159], off
	v_lshl_add_u64 v[158:159], v[158:159], 0, s[72:73]
	s_waitcnt vmcnt(23)
	s_waitcnt lgkmcnt(5)
	v_mfma_f32_32x32x16_f16 v[2:17], v[122:125], v[98:101], v[2:17]
	s_waitcnt lgkmcnt(4)
	v_mfma_f32_32x32x16_f16 v[18:33], v[126:129], v[98:101], v[18:33]
	ds_read_b128 v[122:125], v162 offset:17536
	ds_read_b128 v[126:129], v162 offset:26240
	global_load_dwordx4 v[98:101], v[158:159], off
	v_lshl_add_u64 v[158:159], v[158:159], 0, s[72:73]
	s_waitcnt vmcnt(23)
	s_waitcnt lgkmcnt(5)
	v_mfma_f32_32x32x16_f16 v[2:17], v[130:133], v[102:105], v[2:17]
	s_waitcnt lgkmcnt(4)
	v_mfma_f32_32x32x16_f16 v[18:33], v[134:137], v[102:105], v[18:33]
	ds_read_b128 v[130:133], v162 offset:17568
	ds_read_b128 v[134:137], v162 offset:26272
	global_load_dwordx4 v[102:105], v[158:159], off
	v_lshl_add_u64 v[158:159], v[158:159], 0, s[72:73]
	s_waitcnt vmcnt(23)
	s_waitcnt lgkmcnt(5)
	v_mfma_f32_32x32x16_f16 v[2:17], v[114:117], v[106:109], v[2:17]
	s_waitcnt lgkmcnt(4)
	v_mfma_f32_32x32x16_f16 v[18:33], v[118:121], v[106:109], v[18:33]
	ds_read_b128 v[114:117], v162 offset:17600
	ds_read_b128 v[118:121], v162 offset:26304
	global_load_dwordx4 v[106:109], v[158:159], off
	v_lshl_add_u64 v[158:159], v[158:159], 0, s[72:73]
	s_waitcnt vmcnt(23)
	s_waitcnt lgkmcnt(5)
	v_mfma_f32_32x32x16_f16 v[2:17], v[122:125], v[142:145], v[2:17]
	s_waitcnt lgkmcnt(4)
	v_mfma_f32_32x32x16_f16 v[18:33], v[126:129], v[142:145], v[18:33]
	ds_read_b128 v[122:125], v162 offset:17632
	ds_read_b128 v[126:129], v162 offset:26336
	global_load_dwordx4 v[142:145], v[158:159], off
	v_lshl_add_u64 v[158:159], v[158:159], 0, s[72:73]
	s_waitcnt vmcnt(23)
	s_waitcnt lgkmcnt(5)
	v_mfma_f32_32x32x16_f16 v[2:17], v[130:133], v[146:149], v[2:17]
	s_waitcnt lgkmcnt(4)
	v_mfma_f32_32x32x16_f16 v[18:33], v[134:137], v[146:149], v[18:33]
	global_load_dwordx4 v[146:149], v[158:159], off
	v_lshl_add_u64 v[158:159], v[158:159], 0, s[72:73]
	s_waitcnt vmcnt(23)
	s_waitcnt lgkmcnt(3)
	v_mfma_f32_32x32x16_f16 v[2:17], v[114:117], v[150:153], v[2:17]
	s_waitcnt lgkmcnt(2)
	v_mfma_f32_32x32x16_f16 v[18:33], v[118:121], v[150:153], v[18:33]
	global_load_dwordx4 v[150:153], v[158:159], off
	v_lshl_add_u64 v[158:159], v[158:159], 0, s[72:73]
	s_waitcnt vmcnt(23)
	s_waitcnt lgkmcnt(1)
	v_mfma_f32_32x32x16_f16 v[2:17], v[122:125], v[154:157], v[2:17]
	s_waitcnt lgkmcnt(0)
	v_mfma_f32_32x32x16_f16 v[18:33], v[126:129], v[154:157], v[18:33]
	global_load_dwordx4 v[154:157], v[158:159], off
	v_lshl_add_u64 v[158:159], v[158:159], 0, s[72:73]
	s_waitcnt lgkmcnt(0)
	s_barrier
	ds_read_b128 v[114:117], v162 offset:34816
	ds_read_b128 v[118:121], v162 offset:43520
	ds_read_b128 v[122:125], v162 offset:34848
	ds_read_b128 v[126:129], v162 offset:43552
	ds_read_b128 v[130:133], v162 offset:34880
	ds_read_b128 v[134:137], v162 offset:43584
	s_waitcnt vmcnt(23)
	s_waitcnt lgkmcnt(5)
	v_mfma_f32_32x32x16_f16 v[2:17], v[114:117], v[110:113], v[2:17]
	s_waitcnt lgkmcnt(4)
	v_mfma_f32_32x32x16_f16 v[18:33], v[118:121], v[110:113], v[18:33]
	ds_read_b128 v[114:117], v162 offset:34912
	ds_read_b128 v[118:121], v162 offset:43616
	global_load_dwordx4 v[110:113], v[158:159], off
	v_lshl_add_u64 v[158:159], v[158:159], 0, s[72:73]
	s_waitcnt vmcnt(23)
	s_waitcnt lgkmcnt(5)
	v_mfma_f32_32x32x16_f16 v[2:17], v[122:125], v[90:93], v[2:17]
	s_waitcnt lgkmcnt(4)
	v_mfma_f32_32x32x16_f16 v[18:33], v[126:129], v[90:93], v[18:33]
	ds_read_b128 v[122:125], v162 offset:34944
	ds_read_b128 v[126:129], v162 offset:43648
	global_load_dwordx4 v[90:93], v[158:159], off
	v_lshl_add_u64 v[158:159], v[158:159], 0, s[72:73]
	s_waitcnt vmcnt(23)
	s_waitcnt lgkmcnt(5)
	v_mfma_f32_32x32x16_f16 v[2:17], v[130:133], v[86:89], v[2:17]
	s_waitcnt lgkmcnt(4)
	v_mfma_f32_32x32x16_f16 v[18:33], v[134:137], v[86:89], v[18:33]
	ds_read_b128 v[130:133], v162 offset:34976
	ds_read_b128 v[134:137], v162 offset:43680
	global_load_dwordx4 v[86:89], v[158:159], off
	v_lshl_add_u64 v[158:159], v[158:159], 0, s[72:73]
	s_waitcnt vmcnt(23)
	s_waitcnt lgkmcnt(5)
	v_mfma_f32_32x32x16_f16 v[2:17], v[114:117], v[82:85], v[2:17]
	s_waitcnt lgkmcnt(4)
	v_mfma_f32_32x32x16_f16 v[18:33], v[118:121], v[82:85], v[18:33]
	ds_read_b128 v[114:117], v162 offset:35008
	ds_read_b128 v[118:121], v162 offset:43712
	global_load_dwordx4 v[82:85], v[158:159], off
	v_lshl_add_u64 v[158:159], v[158:159], 0, s[72:73]
	s_waitcnt vmcnt(23)
	s_waitcnt lgkmcnt(5)
	v_mfma_f32_32x32x16_f16 v[2:17], v[122:125], v[78:81], v[2:17]
	s_waitcnt lgkmcnt(4)
	v_mfma_f32_32x32x16_f16 v[18:33], v[126:129], v[78:81], v[18:33]
	ds_read_b128 v[122:125], v162 offset:35040
	ds_read_b128 v[126:129], v162 offset:43744
	global_load_dwordx4 v[78:81], v[158:159], off
	v_lshl_add_u64 v[158:159], v[158:159], 0, s[72:73]
	s_waitcnt vmcnt(23)
	s_waitcnt lgkmcnt(5)
	v_mfma_f32_32x32x16_f16 v[2:17], v[130:133], v[74:77], v[2:17]
	s_waitcnt lgkmcnt(4)
	v_mfma_f32_32x32x16_f16 v[18:33], v[134:137], v[74:77], v[18:33]
	global_load_dwordx4 v[74:77], v[158:159], off
	v_lshl_add_u64 v[158:159], v[158:159], 0, s[72:73]
	s_waitcnt vmcnt(23)
	s_waitcnt lgkmcnt(3)
	v_mfma_f32_32x32x16_f16 v[2:17], v[114:117], v[70:73], v[2:17]
	s_waitcnt lgkmcnt(2)
	v_mfma_f32_32x32x16_f16 v[18:33], v[118:121], v[70:73], v[18:33]
	global_load_dwordx4 v[70:73], v[158:159], off
	v_lshl_add_u64 v[158:159], v[158:159], 0, s[72:73]
	s_waitcnt vmcnt(23)
	s_waitcnt lgkmcnt(1)
	v_mfma_f32_32x32x16_f16 v[2:17], v[122:125], v[66:69], v[2:17]
	s_waitcnt lgkmcnt(0)
	v_mfma_f32_32x32x16_f16 v[18:33], v[126:129], v[66:69], v[18:33]
	global_load_dwordx4 v[66:69], v[158:159], off
	v_lshl_add_u64 v[158:159], v[158:159], 0, s[72:73]
	ds_read_b128 v[114:117], v162 offset:52224
	ds_read_b128 v[118:121], v162 offset:60928
	ds_read_b128 v[122:125], v162 offset:52256
	ds_read_b128 v[126:129], v162 offset:60960
	ds_read_b128 v[130:133], v162 offset:52288
	ds_read_b128 v[134:137], v162 offset:60992
	s_waitcnt vmcnt(23)
	s_waitcnt lgkmcnt(5)
	v_mfma_f32_32x32x16_f16 v[2:17], v[114:117], v[62:65], v[2:17]
	s_waitcnt lgkmcnt(4)
	v_mfma_f32_32x32x16_f16 v[18:33], v[118:121], v[62:65], v[18:33]
	ds_read_b128 v[114:117], v162 offset:52320
	ds_read_b128 v[118:121], v162 offset:61024
	global_load_dwordx4 v[62:65], v[158:159], off
	v_lshl_add_u64 v[158:159], v[158:159], 0, s[72:73]
	s_waitcnt vmcnt(23)
	s_waitcnt lgkmcnt(5)
	v_mfma_f32_32x32x16_f16 v[2:17], v[122:125], v[58:61], v[2:17]
	s_waitcnt lgkmcnt(4)
	v_mfma_f32_32x32x16_f16 v[18:33], v[126:129], v[58:61], v[18:33]
	ds_read_b128 v[122:125], v162 offset:52352
	ds_read_b128 v[126:129], v162 offset:61056
	global_load_dwordx4 v[58:61], v[158:159], off
	v_lshl_add_u64 v[158:159], v[158:159], 0, s[72:73]
	s_waitcnt vmcnt(23)
	s_waitcnt lgkmcnt(5)
	v_mfma_f32_32x32x16_f16 v[2:17], v[130:133], v[54:57], v[2:17]
	s_waitcnt lgkmcnt(4)
	v_mfma_f32_32x32x16_f16 v[18:33], v[134:137], v[54:57], v[18:33]
	ds_read_b128 v[130:133], v162 offset:52384
	ds_read_b128 v[134:137], v162 offset:61088
	global_load_dwordx4 v[54:57], v[158:159], off
	v_lshl_add_u64 v[158:159], v[158:159], 0, s[72:73]
	s_waitcnt vmcnt(23)
	s_waitcnt lgkmcnt(5)
	v_mfma_f32_32x32x16_f16 v[2:17], v[114:117], v[50:53], v[2:17]
	s_waitcnt lgkmcnt(4)
	v_mfma_f32_32x32x16_f16 v[18:33], v[118:121], v[50:53], v[18:33]
	ds_read_b128 v[114:117], v162 offset:52416
	ds_read_b128 v[118:121], v162 offset:61120
	global_load_dwordx4 v[50:53], v[158:159], off
	v_lshl_add_u64 v[158:159], v[158:159], 0, s[72:73]
	s_waitcnt vmcnt(23)
	s_waitcnt lgkmcnt(5)
	v_mfma_f32_32x32x16_f16 v[2:17], v[122:125], v[46:49], v[2:17]
	s_waitcnt lgkmcnt(4)
	v_mfma_f32_32x32x16_f16 v[18:33], v[126:129], v[46:49], v[18:33]
	ds_read_b128 v[122:125], v162 offset:52448
	ds_read_b128 v[126:129], v162 offset:61152
	global_load_dwordx4 v[46:49], v[158:159], off
	v_lshl_add_u64 v[158:159], v[158:159], 0, s[72:73]
	s_waitcnt vmcnt(23)
	s_waitcnt lgkmcnt(5)
	v_mfma_f32_32x32x16_f16 v[2:17], v[130:133], v[42:45], v[2:17]
	s_waitcnt lgkmcnt(4)
	v_mfma_f32_32x32x16_f16 v[18:33], v[134:137], v[42:45], v[18:33]
	global_load_dwordx4 v[42:45], v[158:159], off
	v_lshl_add_u64 v[158:159], v[158:159], 0, s[72:73]
	s_waitcnt vmcnt(23)
	s_waitcnt lgkmcnt(3)
	v_mfma_f32_32x32x16_f16 v[2:17], v[114:117], v[38:41], v[2:17]
	s_waitcnt lgkmcnt(2)
	v_mfma_f32_32x32x16_f16 v[18:33], v[118:121], v[38:41], v[18:33]
	global_load_dwordx4 v[38:41], v[158:159], off
	v_lshl_add_u64 v[158:159], v[158:159], 0, s[72:73]
	s_waitcnt vmcnt(23)
	s_waitcnt lgkmcnt(1)
	v_mfma_f32_32x32x16_f16 v[2:17], v[122:125], v[34:37], v[2:17]
	s_waitcnt lgkmcnt(0)
	v_mfma_f32_32x32x16_f16 v[18:33], v[126:129], v[34:37], v[18:33]
	global_load_dwordx4 v[34:37], v[158:159], off
	v_lshl_add_u64 v[158:159], v[158:159], 0, s[72:73]
	s_waitcnt lgkmcnt(0)
	s_barrier
	ds_read_b128 v[114:117], v163 offset:0
	ds_read_b128 v[118:121], v163 offset:8704
	ds_read_b128 v[122:125], v163 offset:32
	ds_read_b128 v[126:129], v163 offset:8736
	ds_read_b128 v[130:133], v163 offset:64
	ds_read_b128 v[134:137], v163 offset:8768
	s_waitcnt vmcnt(23)
	s_waitcnt lgkmcnt(5)
	v_mfma_f32_32x32x16_f16 v[2:17], v[114:117], v[94:97], v[2:17]
	s_waitcnt lgkmcnt(4)
	v_mfma_f32_32x32x16_f16 v[18:33], v[118:121], v[94:97], v[18:33]
	ds_read_b128 v[114:117], v163 offset:96
	ds_read_b128 v[118:121], v163 offset:8800
	global_load_dwordx4 v[94:97], v[158:159], off
	v_lshl_add_u64 v[158:159], v[158:159], 0, s[72:73]
	s_waitcnt vmcnt(23)
	s_waitcnt lgkmcnt(5)
	v_mfma_f32_32x32x16_f16 v[2:17], v[122:125], v[98:101], v[2:17]
	s_waitcnt lgkmcnt(4)
	v_mfma_f32_32x32x16_f16 v[18:33], v[126:129], v[98:101], v[18:33]
	ds_read_b128 v[122:125], v163 offset:128
	ds_read_b128 v[126:129], v163 offset:8832
	global_load_dwordx4 v[98:101], v[158:159], off
	v_lshl_add_u64 v[158:159], v[158:159], 0, s[72:73]
	s_waitcnt vmcnt(23)
	s_waitcnt lgkmcnt(5)
	v_mfma_f32_32x32x16_f16 v[2:17], v[130:133], v[102:105], v[2:17]
	s_waitcnt lgkmcnt(4)
	v_mfma_f32_32x32x16_f16 v[18:33], v[134:137], v[102:105], v[18:33]
	ds_read_b128 v[130:133], v163 offset:160
	ds_read_b128 v[134:137], v163 offset:8864
	global_load_dwordx4 v[102:105], v[158:159], off
	v_lshl_add_u64 v[158:159], v[158:159], 0, s[72:73]
	s_waitcnt vmcnt(23)
	s_waitcnt lgkmcnt(5)
	v_mfma_f32_32x32x16_f16 v[2:17], v[114:117], v[106:109], v[2:17]
	s_waitcnt lgkmcnt(4)
	v_mfma_f32_32x32x16_f16 v[18:33], v[118:121], v[106:109], v[18:33]
	ds_read_b128 v[114:117], v163 offset:192
	ds_read_b128 v[118:121], v163 offset:8896
	global_load_dwordx4 v[106:109], v[158:159], off
	v_lshl_add_u64 v[158:159], v[158:159], 0, s[72:73]
	s_waitcnt vmcnt(23)
	s_waitcnt lgkmcnt(5)
	v_mfma_f32_32x32x16_f16 v[2:17], v[122:125], v[142:145], v[2:17]
	s_waitcnt lgkmcnt(4)
	v_mfma_f32_32x32x16_f16 v[18:33], v[126:129], v[142:145], v[18:33]
	ds_read_b128 v[122:125], v163 offset:224
	ds_read_b128 v[126:129], v163 offset:8928
	global_load_dwordx4 v[142:145], v[158:159], off
	v_lshl_add_u64 v[158:159], v[158:159], 0, s[72:73]
	s_waitcnt vmcnt(23)
	s_waitcnt lgkmcnt(5)
	v_mfma_f32_32x32x16_f16 v[2:17], v[130:133], v[146:149], v[2:17]
	s_waitcnt lgkmcnt(4)
	v_mfma_f32_32x32x16_f16 v[18:33], v[134:137], v[146:149], v[18:33]
	global_load_dwordx4 v[146:149], v[158:159], off
	v_lshl_add_u64 v[158:159], v[158:159], 0, s[72:73]
	s_waitcnt vmcnt(23)
	s_waitcnt lgkmcnt(3)
	v_mfma_f32_32x32x16_f16 v[2:17], v[114:117], v[150:153], v[2:17]
	s_waitcnt lgkmcnt(2)
	v_mfma_f32_32x32x16_f16 v[18:33], v[118:121], v[150:153], v[18:33]
	global_load_dwordx4 v[150:153], v[158:159], off
	v_lshl_add_u64 v[158:159], v[158:159], 0, s[72:73]
	s_waitcnt vmcnt(23)
	s_waitcnt lgkmcnt(1)
	v_mfma_f32_32x32x16_f16 v[2:17], v[122:125], v[154:157], v[2:17]
	s_waitcnt lgkmcnt(0)
	v_mfma_f32_32x32x16_f16 v[18:33], v[126:129], v[154:157], v[18:33]
	global_load_dwordx4 v[154:157], v[158:159], off
	v_lshl_add_u64 v[158:159], v[158:159], 0, s[72:73]
	ds_read_b128 v[114:117], v162 offset:0
	ds_read_b128 v[118:121], v162 offset:8704
	ds_read_b128 v[122:125], v162 offset:32
	ds_read_b128 v[126:129], v162 offset:8736
	ds_read_b128 v[130:133], v162 offset:64
	ds_read_b128 v[134:137], v162 offset:8768
	s_waitcnt vmcnt(23)
	s_waitcnt lgkmcnt(5)
	v_mfma_f32_32x32x16_f16 v[2:17], v[114:117], v[110:113], v[2:17]
	s_waitcnt lgkmcnt(4)
	v_mfma_f32_32x32x16_f16 v[18:33], v[118:121], v[110:113], v[18:33]
	ds_read_b128 v[114:117], v162 offset:96
	ds_read_b128 v[118:121], v162 offset:8800
	global_load_dwordx4 v[110:113], v[158:159], off
	v_lshl_add_u64 v[158:159], v[158:159], 0, s[72:73]
	s_waitcnt vmcnt(23)
	s_waitcnt lgkmcnt(5)
	v_mfma_f32_32x32x16_f16 v[2:17], v[122:125], v[90:93], v[2:17]
	s_waitcnt lgkmcnt(4)
	v_mfma_f32_32x32x16_f16 v[18:33], v[126:129], v[90:93], v[18:33]
	ds_read_b128 v[122:125], v162 offset:128
	ds_read_b128 v[126:129], v162 offset:8832
	global_load_dwordx4 v[90:93], v[158:159], off
	v_lshl_add_u64 v[158:159], v[158:159], 0, s[72:73]
	s_waitcnt vmcnt(23)
	s_waitcnt lgkmcnt(5)
	v_mfma_f32_32x32x16_f16 v[2:17], v[130:133], v[86:89], v[2:17]
	s_waitcnt lgkmcnt(4)
	v_mfma_f32_32x32x16_f16 v[18:33], v[134:137], v[86:89], v[18:33]
	ds_read_b128 v[130:133], v162 offset:160
	ds_read_b128 v[134:137], v162 offset:8864
	global_load_dwordx4 v[86:89], v[158:159], off
	v_lshl_add_u64 v[158:159], v[158:159], 0, s[72:73]
	s_waitcnt vmcnt(23)
	s_waitcnt lgkmcnt(5)
	v_mfma_f32_32x32x16_f16 v[2:17], v[114:117], v[82:85], v[2:17]
	s_waitcnt lgkmcnt(4)
	v_mfma_f32_32x32x16_f16 v[18:33], v[118:121], v[82:85], v[18:33]
	ds_read_b128 v[114:117], v162 offset:192
	ds_read_b128 v[118:121], v162 offset:8896
	global_load_dwordx4 v[82:85], v[158:159], off
	v_lshl_add_u64 v[158:159], v[158:159], 0, s[72:73]
	s_waitcnt vmcnt(23)
	s_waitcnt lgkmcnt(5)
	v_mfma_f32_32x32x16_f16 v[2:17], v[122:125], v[78:81], v[2:17]
	s_waitcnt lgkmcnt(4)
	v_mfma_f32_32x32x16_f16 v[18:33], v[126:129], v[78:81], v[18:33]
	ds_read_b128 v[122:125], v162 offset:224
	ds_read_b128 v[126:129], v162 offset:8928
	global_load_dwordx4 v[78:81], v[158:159], off
	v_lshl_add_u64 v[158:159], v[158:159], 0, s[72:73]
	s_waitcnt vmcnt(23)
	s_waitcnt lgkmcnt(5)
	v_mfma_f32_32x32x16_f16 v[2:17], v[130:133], v[74:77], v[2:17]
	s_waitcnt lgkmcnt(4)
	v_mfma_f32_32x32x16_f16 v[18:33], v[134:137], v[74:77], v[18:33]
	global_load_dwordx4 v[74:77], v[158:159], off
	v_lshl_add_u64 v[158:159], v[158:159], 0, s[72:73]
	s_waitcnt vmcnt(23)
	s_waitcnt lgkmcnt(3)
	v_mfma_f32_32x32x16_f16 v[2:17], v[114:117], v[70:73], v[2:17]
	s_waitcnt lgkmcnt(2)
	v_mfma_f32_32x32x16_f16 v[18:33], v[118:121], v[70:73], v[18:33]
	global_load_dwordx4 v[70:73], v[158:159], off
	v_lshl_add_u64 v[158:159], v[158:159], 0, s[72:73]
	s_waitcnt vmcnt(23)
	s_waitcnt lgkmcnt(1)
	v_mfma_f32_32x32x16_f16 v[2:17], v[122:125], v[66:69], v[2:17]
	s_waitcnt lgkmcnt(0)
	v_mfma_f32_32x32x16_f16 v[18:33], v[126:129], v[66:69], v[18:33]
	global_load_dwordx4 v[66:69], v[158:159], off
	v_lshl_add_u64 v[158:159], v[158:159], 0, s[72:73]
	s_waitcnt lgkmcnt(0)
	s_barrier
	ds_read_b128 v[114:117], v162 offset:17408
	ds_read_b128 v[118:121], v162 offset:26112
	ds_read_b128 v[122:125], v162 offset:17440
	ds_read_b128 v[126:129], v162 offset:26144
	ds_read_b128 v[130:133], v162 offset:17472
	ds_read_b128 v[134:137], v162 offset:26176
	s_waitcnt vmcnt(23)
	s_waitcnt lgkmcnt(5)
	v_mfma_f32_32x32x16_f16 v[2:17], v[114:117], v[62:65], v[2:17]
	s_waitcnt lgkmcnt(4)
	v_mfma_f32_32x32x16_f16 v[18:33], v[118:121], v[62:65], v[18:33]
	ds_read_b128 v[114:117], v162 offset:17504
	ds_read_b128 v[118:121], v162 offset:26208
	global_load_dwordx4 v[62:65], v[158:159], off
	v_lshl_add_u64 v[158:159], v[158:159], 0, s[72:73]
	s_waitcnt vmcnt(23)
	s_waitcnt lgkmcnt(5)
	v_mfma_f32_32x32x16_f16 v[2:17], v[122:125], v[58:61], v[2:17]
	s_waitcnt lgkmcnt(4)
	v_mfma_f32_32x32x16_f16 v[18:33], v[126:129], v[58:61], v[18:33]
	ds_read_b128 v[122:125], v162 offset:17536
	ds_read_b128 v[126:129], v162 offset:26240
	global_load_dwordx4 v[58:61], v[158:159], off
	v_lshl_add_u64 v[158:159], v[158:159], 0, s[72:73]
	s_waitcnt vmcnt(23)
	s_waitcnt lgkmcnt(5)
	v_mfma_f32_32x32x16_f16 v[2:17], v[130:133], v[54:57], v[2:17]
	s_waitcnt lgkmcnt(4)
	v_mfma_f32_32x32x16_f16 v[18:33], v[134:137], v[54:57], v[18:33]
	ds_read_b128 v[130:133], v162 offset:17568
	ds_read_b128 v[134:137], v162 offset:26272
	global_load_dwordx4 v[54:57], v[158:159], off
	v_lshl_add_u64 v[158:159], v[158:159], 0, s[72:73]
	s_waitcnt vmcnt(23)
	s_waitcnt lgkmcnt(5)
	v_mfma_f32_32x32x16_f16 v[2:17], v[114:117], v[50:53], v[2:17]
	s_waitcnt lgkmcnt(4)
	v_mfma_f32_32x32x16_f16 v[18:33], v[118:121], v[50:53], v[18:33]
	ds_read_b128 v[114:117], v162 offset:17600
	ds_read_b128 v[118:121], v162 offset:26304
	global_load_dwordx4 v[50:53], v[158:159], off
	v_lshl_add_u64 v[158:159], v[158:159], 0, s[72:73]
	s_waitcnt vmcnt(23)
	s_waitcnt lgkmcnt(5)
	v_mfma_f32_32x32x16_f16 v[2:17], v[122:125], v[46:49], v[2:17]
	s_waitcnt lgkmcnt(4)
	v_mfma_f32_32x32x16_f16 v[18:33], v[126:129], v[46:49], v[18:33]
	ds_read_b128 v[122:125], v162 offset:17632
	ds_read_b128 v[126:129], v162 offset:26336
	global_load_dwordx4 v[46:49], v[158:159], off
	v_lshl_add_u64 v[158:159], v[158:159], 0, s[72:73]
	s_waitcnt vmcnt(23)
	s_waitcnt lgkmcnt(5)
	v_mfma_f32_32x32x16_f16 v[2:17], v[130:133], v[42:45], v[2:17]
	s_waitcnt lgkmcnt(4)
	v_mfma_f32_32x32x16_f16 v[18:33], v[134:137], v[42:45], v[18:33]
	global_load_dwordx4 v[42:45], v[158:159], off
	v_lshl_add_u64 v[158:159], v[158:159], 0, s[72:73]
	s_waitcnt vmcnt(23)
	s_waitcnt lgkmcnt(3)
	v_mfma_f32_32x32x16_f16 v[2:17], v[114:117], v[38:41], v[2:17]
	s_waitcnt lgkmcnt(2)
	v_mfma_f32_32x32x16_f16 v[18:33], v[118:121], v[38:41], v[18:33]
	global_load_dwordx4 v[38:41], v[158:159], off
	v_lshl_add_u64 v[158:159], v[158:159], 0, s[72:73]
	s_waitcnt vmcnt(23)
	s_waitcnt lgkmcnt(1)
	v_mfma_f32_32x32x16_f16 v[2:17], v[122:125], v[34:37], v[2:17]
	s_waitcnt lgkmcnt(0)
	v_mfma_f32_32x32x16_f16 v[18:33], v[126:129], v[34:37], v[18:33]
	global_load_dwordx4 v[34:37], v[158:159], off
	v_lshl_add_u64 v[158:159], v[158:159], 0, s[72:73]
	ds_read_b128 v[114:117], v162 offset:34816
	ds_read_b128 v[118:121], v162 offset:43520
	ds_read_b128 v[122:125], v162 offset:34848
	ds_read_b128 v[126:129], v162 offset:43552
	ds_read_b128 v[130:133], v162 offset:34880
	ds_read_b128 v[134:137], v162 offset:43584
	s_waitcnt vmcnt(23)
	s_waitcnt lgkmcnt(5)
	v_mfma_f32_32x32x16_f16 v[2:17], v[114:117], v[94:97], v[2:17]
	s_waitcnt lgkmcnt(4)
	v_mfma_f32_32x32x16_f16 v[18:33], v[118:121], v[94:97], v[18:33]
	ds_read_b128 v[114:117], v162 offset:34912
	ds_read_b128 v[118:121], v162 offset:43616
	global_load_dwordx4 v[94:97], v[158:159], off
	v_lshl_add_u64 v[158:159], v[158:159], 0, s[72:73]
	s_waitcnt vmcnt(23)
	s_waitcnt lgkmcnt(5)
	v_mfma_f32_32x32x16_f16 v[2:17], v[122:125], v[98:101], v[2:17]
	s_waitcnt lgkmcnt(4)
	v_mfma_f32_32x32x16_f16 v[18:33], v[126:129], v[98:101], v[18:33]
	ds_read_b128 v[122:125], v162 offset:34944
	ds_read_b128 v[126:129], v162 offset:43648
	global_load_dwordx4 v[98:101], v[158:159], off
	v_lshl_add_u64 v[158:159], v[158:159], 0, s[72:73]
	s_waitcnt vmcnt(23)
	s_waitcnt lgkmcnt(5)
	v_mfma_f32_32x32x16_f16 v[2:17], v[130:133], v[102:105], v[2:17]
	s_waitcnt lgkmcnt(4)
	v_mfma_f32_32x32x16_f16 v[18:33], v[134:137], v[102:105], v[18:33]
	ds_read_b128 v[130:133], v162 offset:34976
	ds_read_b128 v[134:137], v162 offset:43680
	global_load_dwordx4 v[102:105], v[158:159], off
	v_lshl_add_u64 v[158:159], v[158:159], 0, s[72:73]
	s_waitcnt vmcnt(23)
	s_waitcnt lgkmcnt(5)
	v_mfma_f32_32x32x16_f16 v[2:17], v[114:117], v[106:109], v[2:17]
	s_waitcnt lgkmcnt(4)
	v_mfma_f32_32x32x16_f16 v[18:33], v[118:121], v[106:109], v[18:33]
	ds_read_b128 v[114:117], v162 offset:35008
	ds_read_b128 v[118:121], v162 offset:43712
	global_load_dwordx4 v[106:109], v[158:159], off
	v_lshl_add_u64 v[158:159], v[158:159], 0, s[72:73]
	s_waitcnt vmcnt(23)
	s_waitcnt lgkmcnt(5)
	v_mfma_f32_32x32x16_f16 v[2:17], v[122:125], v[142:145], v[2:17]
	s_waitcnt lgkmcnt(4)
	v_mfma_f32_32x32x16_f16 v[18:33], v[126:129], v[142:145], v[18:33]
	ds_read_b128 v[122:125], v162 offset:35040
	ds_read_b128 v[126:129], v162 offset:43744
	global_load_dwordx4 v[142:145], v[158:159], off
	v_lshl_add_u64 v[158:159], v[158:159], 0, s[72:73]
	s_waitcnt vmcnt(23)
	s_waitcnt lgkmcnt(5)
	v_mfma_f32_32x32x16_f16 v[2:17], v[130:133], v[146:149], v[2:17]
	s_waitcnt lgkmcnt(4)
	v_mfma_f32_32x32x16_f16 v[18:33], v[134:137], v[146:149], v[18:33]
	global_load_dwordx4 v[146:149], v[158:159], off
	v_lshl_add_u64 v[158:159], v[158:159], 0, s[72:73]
	s_waitcnt vmcnt(23)
	s_waitcnt lgkmcnt(3)
	v_mfma_f32_32x32x16_f16 v[2:17], v[114:117], v[150:153], v[2:17]
	s_waitcnt lgkmcnt(2)
	v_mfma_f32_32x32x16_f16 v[18:33], v[118:121], v[150:153], v[18:33]
	global_load_dwordx4 v[150:153], v[158:159], off
	v_lshl_add_u64 v[158:159], v[158:159], 0, s[72:73]
	s_waitcnt vmcnt(23)
	s_waitcnt lgkmcnt(1)
	v_mfma_f32_32x32x16_f16 v[2:17], v[122:125], v[154:157], v[2:17]
	s_waitcnt lgkmcnt(0)
	v_mfma_f32_32x32x16_f16 v[18:33], v[126:129], v[154:157], v[18:33]
	global_load_dwordx4 v[154:157], v[158:159], off
	v_lshl_add_u64 v[158:159], v[158:159], 0, s[72:73]
	s_waitcnt lgkmcnt(0)
	s_barrier
	ds_read_b128 v[114:117], v162 offset:52224
	ds_read_b128 v[118:121], v162 offset:60928
	ds_read_b128 v[122:125], v162 offset:52256
	ds_read_b128 v[126:129], v162 offset:60960
	ds_read_b128 v[130:133], v162 offset:52288
	ds_read_b128 v[134:137], v162 offset:60992
	s_waitcnt vmcnt(23)
	s_waitcnt lgkmcnt(5)
	v_mfma_f32_32x32x16_f16 v[2:17], v[114:117], v[110:113], v[2:17]
	s_waitcnt lgkmcnt(4)
	v_mfma_f32_32x32x16_f16 v[18:33], v[118:121], v[110:113], v[18:33]
	ds_read_b128 v[114:117], v162 offset:52320
	ds_read_b128 v[118:121], v162 offset:61024
	global_load_dwordx4 v[110:113], v[158:159], off
	v_lshl_add_u64 v[158:159], v[158:159], 0, s[72:73]
	s_waitcnt vmcnt(23)
	s_waitcnt lgkmcnt(5)
	v_mfma_f32_32x32x16_f16 v[2:17], v[122:125], v[90:93], v[2:17]
	s_waitcnt lgkmcnt(4)
	v_mfma_f32_32x32x16_f16 v[18:33], v[126:129], v[90:93], v[18:33]
	ds_read_b128 v[122:125], v162 offset:52352
	ds_read_b128 v[126:129], v162 offset:61056
	global_load_dwordx4 v[90:93], v[158:159], off
	v_lshl_add_u64 v[158:159], v[158:159], 0, s[72:73]
	s_waitcnt vmcnt(23)
	s_waitcnt lgkmcnt(5)
	v_mfma_f32_32x32x16_f16 v[2:17], v[130:133], v[86:89], v[2:17]
	s_waitcnt lgkmcnt(4)
	v_mfma_f32_32x32x16_f16 v[18:33], v[134:137], v[86:89], v[18:33]
	ds_read_b128 v[130:133], v162 offset:52384
	ds_read_b128 v[134:137], v162 offset:61088
	global_load_dwordx4 v[86:89], v[158:159], off
	v_lshl_add_u64 v[158:159], v[158:159], 0, s[72:73]
	s_waitcnt vmcnt(23)
	s_waitcnt lgkmcnt(5)
	v_mfma_f32_32x32x16_f16 v[2:17], v[114:117], v[82:85], v[2:17]
	s_waitcnt lgkmcnt(4)
	v_mfma_f32_32x32x16_f16 v[18:33], v[118:121], v[82:85], v[18:33]
	ds_read_b128 v[114:117], v162 offset:52416
	ds_read_b128 v[118:121], v162 offset:61120
	global_load_dwordx4 v[82:85], v[158:159], off
	v_lshl_add_u64 v[158:159], v[158:159], 0, s[72:73]
	s_waitcnt vmcnt(23)
	s_waitcnt lgkmcnt(5)
	v_mfma_f32_32x32x16_f16 v[2:17], v[122:125], v[78:81], v[2:17]
	s_waitcnt lgkmcnt(4)
	v_mfma_f32_32x32x16_f16 v[18:33], v[126:129], v[78:81], v[18:33]
	ds_read_b128 v[122:125], v162 offset:52448
	ds_read_b128 v[126:129], v162 offset:61152
	global_load_dwordx4 v[78:81], v[158:159], off
	v_lshl_add_u64 v[158:159], v[158:159], 0, s[72:73]
	s_waitcnt vmcnt(23)
	s_waitcnt lgkmcnt(5)
	v_mfma_f32_32x32x16_f16 v[2:17], v[130:133], v[74:77], v[2:17]
	s_waitcnt lgkmcnt(4)
	v_mfma_f32_32x32x16_f16 v[18:33], v[134:137], v[74:77], v[18:33]
	global_load_dwordx4 v[74:77], v[158:159], off
	v_lshl_add_u64 v[158:159], v[158:159], 0, s[72:73]
	s_waitcnt vmcnt(23)
	s_waitcnt lgkmcnt(3)
	v_mfma_f32_32x32x16_f16 v[2:17], v[114:117], v[70:73], v[2:17]
	s_waitcnt lgkmcnt(2)
	v_mfma_f32_32x32x16_f16 v[18:33], v[118:121], v[70:73], v[18:33]
	global_load_dwordx4 v[70:73], v[158:159], off
	v_lshl_add_u64 v[158:159], v[158:159], 0, s[72:73]
	s_waitcnt vmcnt(23)
	s_waitcnt lgkmcnt(1)
	v_mfma_f32_32x32x16_f16 v[2:17], v[122:125], v[66:69], v[2:17]
	s_waitcnt lgkmcnt(0)
	v_mfma_f32_32x32x16_f16 v[18:33], v[126:129], v[66:69], v[18:33]
	global_load_dwordx4 v[66:69], v[158:159], off
	v_lshl_add_u64 v[158:159], v[158:159], 0, s[72:73]
	ds_read_b128 v[114:117], v163 offset:0
	ds_read_b128 v[118:121], v163 offset:8704
	ds_read_b128 v[122:125], v163 offset:32
	ds_read_b128 v[126:129], v163 offset:8736
	ds_read_b128 v[130:133], v163 offset:64
	ds_read_b128 v[134:137], v163 offset:8768
	s_waitcnt vmcnt(23)
	s_waitcnt lgkmcnt(5)
	v_mfma_f32_32x32x16_f16 v[2:17], v[114:117], v[62:65], v[2:17]
	s_waitcnt lgkmcnt(4)
	v_mfma_f32_32x32x16_f16 v[18:33], v[118:121], v[62:65], v[18:33]
	ds_read_b128 v[114:117], v163 offset:96
	ds_read_b128 v[118:121], v163 offset:8800
	global_load_dwordx4 v[62:65], v[158:159], off
	v_lshl_add_u64 v[158:159], v[158:159], 0, s[72:73]
	s_waitcnt vmcnt(23)
	s_waitcnt lgkmcnt(5)
	v_mfma_f32_32x32x16_f16 v[2:17], v[122:125], v[58:61], v[2:17]
	s_waitcnt lgkmcnt(4)
	v_mfma_f32_32x32x16_f16 v[18:33], v[126:129], v[58:61], v[18:33]
	ds_read_b128 v[122:125], v163 offset:128
	ds_read_b128 v[126:129], v163 offset:8832
	global_load_dwordx4 v[58:61], v[158:159], off
	v_lshl_add_u64 v[158:159], v[158:159], 0, s[72:73]
	s_waitcnt vmcnt(23)
	s_waitcnt lgkmcnt(5)
	v_mfma_f32_32x32x16_f16 v[2:17], v[130:133], v[54:57], v[2:17]
	s_waitcnt lgkmcnt(4)
	v_mfma_f32_32x32x16_f16 v[18:33], v[134:137], v[54:57], v[18:33]
	ds_read_b128 v[130:133], v163 offset:160
	ds_read_b128 v[134:137], v163 offset:8864
	global_load_dwordx4 v[54:57], v[158:159], off
	v_lshl_add_u64 v[158:159], v[158:159], 0, s[72:73]
	s_waitcnt vmcnt(23)
	s_waitcnt lgkmcnt(5)
	v_mfma_f32_32x32x16_f16 v[2:17], v[114:117], v[50:53], v[2:17]
	s_waitcnt lgkmcnt(4)
	v_mfma_f32_32x32x16_f16 v[18:33], v[118:121], v[50:53], v[18:33]
	ds_read_b128 v[114:117], v163 offset:192
	ds_read_b128 v[118:121], v163 offset:8896
	global_load_dwordx4 v[50:53], v[158:159], off
	v_lshl_add_u64 v[158:159], v[158:159], 0, s[72:73]
	s_waitcnt vmcnt(23)
	s_waitcnt lgkmcnt(5)
	v_mfma_f32_32x32x16_f16 v[2:17], v[122:125], v[46:49], v[2:17]
	s_waitcnt lgkmcnt(4)
	v_mfma_f32_32x32x16_f16 v[18:33], v[126:129], v[46:49], v[18:33]
	ds_read_b128 v[122:125], v163 offset:224
	ds_read_b128 v[126:129], v163 offset:8928
	global_load_dwordx4 v[46:49], v[158:159], off
	v_lshl_add_u64 v[158:159], v[158:159], 0, s[72:73]
	s_waitcnt vmcnt(23)
	s_waitcnt lgkmcnt(5)
	v_mfma_f32_32x32x16_f16 v[2:17], v[130:133], v[42:45], v[2:17]
	s_waitcnt lgkmcnt(4)
	v_mfma_f32_32x32x16_f16 v[18:33], v[134:137], v[42:45], v[18:33]
	global_load_dwordx4 v[42:45], v[158:159], off
	v_lshl_add_u64 v[158:159], v[158:159], 0, s[72:73]
	s_waitcnt vmcnt(23)
	s_waitcnt lgkmcnt(3)
	v_mfma_f32_32x32x16_f16 v[2:17], v[114:117], v[38:41], v[2:17]
	s_waitcnt lgkmcnt(2)
	v_mfma_f32_32x32x16_f16 v[18:33], v[118:121], v[38:41], v[18:33]
	global_load_dwordx4 v[38:41], v[158:159], off
	v_lshl_add_u64 v[158:159], v[158:159], 0, s[72:73]
	s_waitcnt vmcnt(23)
	s_waitcnt lgkmcnt(1)
	v_mfma_f32_32x32x16_f16 v[2:17], v[122:125], v[34:37], v[2:17]
	s_waitcnt lgkmcnt(0)
	v_mfma_f32_32x32x16_f16 v[18:33], v[126:129], v[34:37], v[18:33]
	global_load_dwordx4 v[34:37], v[158:159], off
	v_lshl_add_u64 v[158:159], v[158:159], 0, s[72:73]
	s_waitcnt lgkmcnt(0)
	s_barrier
	ds_read_b128 v[114:117], v162 offset:0
	ds_read_b128 v[118:121], v162 offset:8704
	ds_read_b128 v[122:125], v162 offset:32
	ds_read_b128 v[126:129], v162 offset:8736
	ds_read_b128 v[130:133], v162 offset:64
	ds_read_b128 v[134:137], v162 offset:8768
	s_waitcnt vmcnt(23)
	s_waitcnt lgkmcnt(5)
	v_mfma_f32_32x32x16_f16 v[2:17], v[114:117], v[94:97], v[2:17]
	s_waitcnt lgkmcnt(4)
	v_mfma_f32_32x32x16_f16 v[18:33], v[118:121], v[94:97], v[18:33]
	ds_read_b128 v[114:117], v162 offset:96
	ds_read_b128 v[118:121], v162 offset:8800
	global_load_dwordx4 v[94:97], v[158:159], off
	v_lshl_add_u64 v[158:159], v[158:159], 0, s[72:73]
	s_waitcnt vmcnt(23)
	s_waitcnt lgkmcnt(5)
	v_mfma_f32_32x32x16_f16 v[2:17], v[122:125], v[98:101], v[2:17]
	s_waitcnt lgkmcnt(4)
	v_mfma_f32_32x32x16_f16 v[18:33], v[126:129], v[98:101], v[18:33]
	ds_read_b128 v[122:125], v162 offset:128
	ds_read_b128 v[126:129], v162 offset:8832
	global_load_dwordx4 v[98:101], v[158:159], off
	v_lshl_add_u64 v[158:159], v[158:159], 0, s[72:73]
	s_waitcnt vmcnt(23)
	s_waitcnt lgkmcnt(5)
	v_mfma_f32_32x32x16_f16 v[2:17], v[130:133], v[102:105], v[2:17]
	s_waitcnt lgkmcnt(4)
	v_mfma_f32_32x32x16_f16 v[18:33], v[134:137], v[102:105], v[18:33]
	ds_read_b128 v[130:133], v162 offset:160
	ds_read_b128 v[134:137], v162 offset:8864
	global_load_dwordx4 v[102:105], v[158:159], off
	v_lshl_add_u64 v[158:159], v[158:159], 0, s[72:73]
	s_waitcnt vmcnt(23)
	s_waitcnt lgkmcnt(5)
	v_mfma_f32_32x32x16_f16 v[2:17], v[114:117], v[106:109], v[2:17]
	s_waitcnt lgkmcnt(4)
	v_mfma_f32_32x32x16_f16 v[18:33], v[118:121], v[106:109], v[18:33]
	ds_read_b128 v[114:117], v162 offset:192
	ds_read_b128 v[118:121], v162 offset:8896
	global_load_dwordx4 v[106:109], v[158:159], off
	v_lshl_add_u64 v[158:159], v[158:159], 0, s[72:73]
	s_waitcnt vmcnt(23)
	s_waitcnt lgkmcnt(5)
	v_mfma_f32_32x32x16_f16 v[2:17], v[122:125], v[142:145], v[2:17]
	s_waitcnt lgkmcnt(4)
	v_mfma_f32_32x32x16_f16 v[18:33], v[126:129], v[142:145], v[18:33]
	ds_read_b128 v[122:125], v162 offset:224
	ds_read_b128 v[126:129], v162 offset:8928
	global_load_dwordx4 v[142:145], v[158:159], off
	v_lshl_add_u64 v[158:159], v[158:159], 0, s[72:73]
	s_waitcnt vmcnt(23)
	s_waitcnt lgkmcnt(5)
	v_mfma_f32_32x32x16_f16 v[2:17], v[130:133], v[146:149], v[2:17]
	s_waitcnt lgkmcnt(4)
	v_mfma_f32_32x32x16_f16 v[18:33], v[134:137], v[146:149], v[18:33]
	global_load_dwordx4 v[146:149], v[158:159], off
	v_lshl_add_u64 v[158:159], v[158:159], 0, s[72:73]
	s_waitcnt vmcnt(23)
	s_waitcnt lgkmcnt(3)
	v_mfma_f32_32x32x16_f16 v[2:17], v[114:117], v[150:153], v[2:17]
	s_waitcnt lgkmcnt(2)
	v_mfma_f32_32x32x16_f16 v[18:33], v[118:121], v[150:153], v[18:33]
	global_load_dwordx4 v[150:153], v[158:159], off
	v_lshl_add_u64 v[158:159], v[158:159], 0, s[72:73]
	s_waitcnt vmcnt(23)
	s_waitcnt lgkmcnt(1)
	v_mfma_f32_32x32x16_f16 v[2:17], v[122:125], v[154:157], v[2:17]
	s_waitcnt lgkmcnt(0)
	v_mfma_f32_32x32x16_f16 v[18:33], v[126:129], v[154:157], v[18:33]
	global_load_dwordx4 v[154:157], v[158:159], off
	v_lshl_add_u64 v[158:159], v[158:159], 0, s[72:73]
	ds_read_b128 v[114:117], v162 offset:17408
	ds_read_b128 v[118:121], v162 offset:26112
	ds_read_b128 v[122:125], v162 offset:17440
	ds_read_b128 v[126:129], v162 offset:26144
	ds_read_b128 v[130:133], v162 offset:17472
	ds_read_b128 v[134:137], v162 offset:26176
	s_waitcnt vmcnt(23)
	s_waitcnt lgkmcnt(5)
	v_mfma_f32_32x32x16_f16 v[2:17], v[114:117], v[110:113], v[2:17]
	s_waitcnt lgkmcnt(4)
	v_mfma_f32_32x32x16_f16 v[18:33], v[118:121], v[110:113], v[18:33]
	ds_read_b128 v[114:117], v162 offset:17504
	ds_read_b128 v[118:121], v162 offset:26208
	s_waitcnt vmcnt(22)
	s_waitcnt lgkmcnt(5)
	v_mfma_f32_32x32x16_f16 v[2:17], v[122:125], v[90:93], v[2:17]
	s_waitcnt lgkmcnt(4)
	v_mfma_f32_32x32x16_f16 v[18:33], v[126:129], v[90:93], v[18:33]
	ds_read_b128 v[122:125], v162 offset:17536
	ds_read_b128 v[126:129], v162 offset:26240
	s_waitcnt vmcnt(21)
	s_waitcnt lgkmcnt(5)
	v_mfma_f32_32x32x16_f16 v[2:17], v[130:133], v[86:89], v[2:17]
	s_waitcnt lgkmcnt(4)
	v_mfma_f32_32x32x16_f16 v[18:33], v[134:137], v[86:89], v[18:33]
	ds_read_b128 v[130:133], v162 offset:17568
	ds_read_b128 v[134:137], v162 offset:26272
	s_waitcnt vmcnt(20)
	s_waitcnt lgkmcnt(5)
	v_mfma_f32_32x32x16_f16 v[2:17], v[114:117], v[82:85], v[2:17]
	s_waitcnt lgkmcnt(4)
	v_mfma_f32_32x32x16_f16 v[18:33], v[118:121], v[82:85], v[18:33]
	ds_read_b128 v[114:117], v162 offset:17600
	ds_read_b128 v[118:121], v162 offset:26304
	s_waitcnt vmcnt(19)
	s_waitcnt lgkmcnt(5)
	v_mfma_f32_32x32x16_f16 v[2:17], v[122:125], v[78:81], v[2:17]
	s_waitcnt lgkmcnt(4)
	v_mfma_f32_32x32x16_f16 v[18:33], v[126:129], v[78:81], v[18:33]
	ds_read_b128 v[122:125], v162 offset:17632
	ds_read_b128 v[126:129], v162 offset:26336
	s_waitcnt vmcnt(18)
	s_waitcnt lgkmcnt(5)
	v_mfma_f32_32x32x16_f16 v[2:17], v[130:133], v[74:77], v[2:17]
	s_waitcnt lgkmcnt(4)
	v_mfma_f32_32x32x16_f16 v[18:33], v[134:137], v[74:77], v[18:33]
	s_waitcnt vmcnt(17)
	s_waitcnt lgkmcnt(3)
	v_mfma_f32_32x32x16_f16 v[2:17], v[114:117], v[70:73], v[2:17]
	s_waitcnt lgkmcnt(2)
	v_mfma_f32_32x32x16_f16 v[18:33], v[118:121], v[70:73], v[18:33]
	s_waitcnt vmcnt(16)
	s_waitcnt lgkmcnt(1)
	v_mfma_f32_32x32x16_f16 v[2:17], v[122:125], v[66:69], v[2:17]
	s_waitcnt lgkmcnt(0)
	v_mfma_f32_32x32x16_f16 v[18:33], v[126:129], v[66:69], v[18:33]
	s_waitcnt lgkmcnt(0)
	s_barrier
	ds_read_b128 v[114:117], v162 offset:34816
	ds_read_b128 v[118:121], v162 offset:43520
	ds_read_b128 v[122:125], v162 offset:34848
	ds_read_b128 v[126:129], v162 offset:43552
	ds_read_b128 v[130:133], v162 offset:34880
	ds_read_b128 v[134:137], v162 offset:43584
	s_waitcnt vmcnt(15)
	s_waitcnt lgkmcnt(5)
	v_mfma_f32_32x32x16_f16 v[2:17], v[114:117], v[62:65], v[2:17]
	s_waitcnt lgkmcnt(4)
	v_mfma_f32_32x32x16_f16 v[18:33], v[118:121], v[62:65], v[18:33]
	ds_read_b128 v[114:117], v162 offset:34912
	ds_read_b128 v[118:121], v162 offset:43616
	s_waitcnt vmcnt(14)
	s_waitcnt lgkmcnt(5)
	v_mfma_f32_32x32x16_f16 v[2:17], v[122:125], v[58:61], v[2:17]
	s_waitcnt lgkmcnt(4)
	v_mfma_f32_32x32x16_f16 v[18:33], v[126:129], v[58:61], v[18:33]
	ds_read_b128 v[122:125], v162 offset:34944
	ds_read_b128 v[126:129], v162 offset:43648
	s_waitcnt vmcnt(13)
	s_waitcnt lgkmcnt(5)
	v_mfma_f32_32x32x16_f16 v[2:17], v[130:133], v[54:57], v[2:17]
	s_waitcnt lgkmcnt(4)
	v_mfma_f32_32x32x16_f16 v[18:33], v[134:137], v[54:57], v[18:33]
	ds_read_b128 v[130:133], v162 offset:34976
	ds_read_b128 v[134:137], v162 offset:43680
	s_waitcnt vmcnt(12)
	s_waitcnt lgkmcnt(5)
	v_mfma_f32_32x32x16_f16 v[2:17], v[114:117], v[50:53], v[2:17]
	s_waitcnt lgkmcnt(4)
	v_mfma_f32_32x32x16_f16 v[18:33], v[118:121], v[50:53], v[18:33]
	ds_read_b128 v[114:117], v162 offset:35008
	ds_read_b128 v[118:121], v162 offset:43712
	s_waitcnt vmcnt(11)
	s_waitcnt lgkmcnt(5)
	v_mfma_f32_32x32x16_f16 v[2:17], v[122:125], v[46:49], v[2:17]
	s_waitcnt lgkmcnt(4)
	v_mfma_f32_32x32x16_f16 v[18:33], v[126:129], v[46:49], v[18:33]
	ds_read_b128 v[122:125], v162 offset:35040
	ds_read_b128 v[126:129], v162 offset:43744
	s_waitcnt vmcnt(10)
	s_waitcnt lgkmcnt(5)
	v_mfma_f32_32x32x16_f16 v[2:17], v[130:133], v[42:45], v[2:17]
	s_waitcnt lgkmcnt(4)
	v_mfma_f32_32x32x16_f16 v[18:33], v[134:137], v[42:45], v[18:33]
	s_waitcnt vmcnt(9)
	s_waitcnt lgkmcnt(3)
	v_mfma_f32_32x32x16_f16 v[2:17], v[114:117], v[38:41], v[2:17]
	s_waitcnt lgkmcnt(2)
	v_mfma_f32_32x32x16_f16 v[18:33], v[118:121], v[38:41], v[18:33]
	s_waitcnt vmcnt(8)
	s_waitcnt lgkmcnt(1)
	v_mfma_f32_32x32x16_f16 v[2:17], v[122:125], v[34:37], v[2:17]
	s_waitcnt lgkmcnt(0)
	v_mfma_f32_32x32x16_f16 v[18:33], v[126:129], v[34:37], v[18:33]
	ds_read_b128 v[114:117], v162 offset:52224
	ds_read_b128 v[118:121], v162 offset:60928
	ds_read_b128 v[122:125], v162 offset:52256
	ds_read_b128 v[126:129], v162 offset:60960
	ds_read_b128 v[130:133], v162 offset:52288
	ds_read_b128 v[134:137], v162 offset:60992
	s_waitcnt vmcnt(7)
	s_waitcnt lgkmcnt(5)
	v_mfma_f32_32x32x16_f16 v[2:17], v[114:117], v[94:97], v[2:17]
	s_waitcnt lgkmcnt(4)
	v_mfma_f32_32x32x16_f16 v[18:33], v[118:121], v[94:97], v[18:33]
	ds_read_b128 v[114:117], v162 offset:52320
	ds_read_b128 v[118:121], v162 offset:61024
	s_waitcnt vmcnt(6)
	s_waitcnt lgkmcnt(5)
	v_mfma_f32_32x32x16_f16 v[2:17], v[122:125], v[98:101], v[2:17]
	s_waitcnt lgkmcnt(4)
	v_mfma_f32_32x32x16_f16 v[18:33], v[126:129], v[98:101], v[18:33]
	ds_read_b128 v[122:125], v162 offset:52352
	ds_read_b128 v[126:129], v162 offset:61056
	s_waitcnt vmcnt(5)
	s_waitcnt lgkmcnt(5)
	v_mfma_f32_32x32x16_f16 v[2:17], v[130:133], v[102:105], v[2:17]
	s_waitcnt lgkmcnt(4)
	v_mfma_f32_32x32x16_f16 v[18:33], v[134:137], v[102:105], v[18:33]
	ds_read_b128 v[130:133], v162 offset:52384
	ds_read_b128 v[134:137], v162 offset:61088
	s_waitcnt vmcnt(4)
	s_waitcnt lgkmcnt(5)
	v_mfma_f32_32x32x16_f16 v[2:17], v[114:117], v[106:109], v[2:17]
	s_waitcnt lgkmcnt(4)
	v_mfma_f32_32x32x16_f16 v[18:33], v[118:121], v[106:109], v[18:33]
	ds_read_b128 v[114:117], v162 offset:52416
	ds_read_b128 v[118:121], v162 offset:61120
	s_waitcnt vmcnt(3)
	s_waitcnt lgkmcnt(5)
	v_mfma_f32_32x32x16_f16 v[2:17], v[122:125], v[142:145], v[2:17]
	s_waitcnt lgkmcnt(4)
	v_mfma_f32_32x32x16_f16 v[18:33], v[126:129], v[142:145], v[18:33]
	ds_read_b128 v[122:125], v162 offset:52448
	ds_read_b128 v[126:129], v162 offset:61152
	s_waitcnt vmcnt(2)
	s_waitcnt lgkmcnt(5)
	v_mfma_f32_32x32x16_f16 v[2:17], v[130:133], v[146:149], v[2:17]
	s_waitcnt lgkmcnt(4)
	v_mfma_f32_32x32x16_f16 v[18:33], v[134:137], v[146:149], v[18:33]
	s_waitcnt vmcnt(1)
	s_waitcnt lgkmcnt(3)
	v_mfma_f32_32x32x16_f16 v[2:17], v[114:117], v[150:153], v[2:17]
	s_waitcnt lgkmcnt(2)
	v_mfma_f32_32x32x16_f16 v[18:33], v[118:121], v[150:153], v[18:33]
	s_waitcnt vmcnt(0)
	s_waitcnt lgkmcnt(1)
	v_mfma_f32_32x32x16_f16 v[2:17], v[122:125], v[154:157], v[2:17]
	s_waitcnt lgkmcnt(0)
	v_mfma_f32_32x32x16_f16 v[18:33], v[126:129], v[154:157], v[18:33]
	s_waitcnt lgkmcnt(0)
	s_barrier
	s_mov_b32 s2, 0x3d800000
	v_mul_u32_u24_e32 v1, 0x420, v1
	v_or_b32_e32 v34, v161, v160
	v_lshlrev_b32_e32 v34, 1, v34
	v_lshl_add_u32 v1, v1, 1, v34
	s_nop 7
	s_nop 7
	v_fma_mixlo_f16 v2, v2, s2, 0
	ds_write_b16 v1, v2
	v_fma_mixlo_f16 v2, v18, s2, 0
	ds_write_b16 v1, v2 offset:16896
	v_fma_mixlo_f16 v2, v3, s2, 0
	ds_write_b16 v1, v2 offset:528
	v_fma_mixlo_f16 v2, v19, s2, 0
	ds_write_b16 v1, v2 offset:17424
	v_fma_mixlo_f16 v2, v4, s2, 0
	ds_write_b16 v1, v2 offset:1056
	v_fma_mixlo_f16 v2, v20, s2, 0
	ds_write_b16 v1, v2 offset:17952
	v_fma_mixlo_f16 v2, v5, s2, 0
	ds_write_b16 v1, v2 offset:1584
	v_fma_mixlo_f16 v2, v21, s2, 0
	ds_write_b16 v1, v2 offset:18480
	v_fma_mixlo_f16 v2, v6, s2, 0
	ds_write_b16 v1, v2 offset:4224
	v_fma_mixlo_f16 v2, v22, s2, 0
	ds_write_b16 v1, v2 offset:21120
	v_fma_mixlo_f16 v2, v7, s2, 0
	ds_write_b16 v1, v2 offset:4752
	v_fma_mixlo_f16 v2, v23, s2, 0
	ds_write_b16 v1, v2 offset:21648
	v_fma_mixlo_f16 v2, v8, s2, 0
	ds_write_b16 v1, v2 offset:5280
	v_fma_mixlo_f16 v2, v24, s2, 0
	ds_write_b16 v1, v2 offset:22176
	v_fma_mixlo_f16 v2, v9, s2, 0
	ds_write_b16 v1, v2 offset:5808
	v_fma_mixlo_f16 v2, v25, s2, 0
	ds_write_b16 v1, v2 offset:22704
	v_fma_mixlo_f16 v2, v10, s2, 0
	ds_write_b16 v1, v2 offset:8448
	v_fma_mixlo_f16 v2, v26, s2, 0
	ds_write_b16 v1, v2 offset:25344
	v_fma_mixlo_f16 v2, v11, s2, 0
	ds_write_b16 v1, v2 offset:8976
	v_fma_mixlo_f16 v2, v27, s2, 0
	ds_write_b16 v1, v2 offset:25872
	v_fma_mixlo_f16 v2, v12, s2, 0
	ds_write_b16 v1, v2 offset:9504
	v_fma_mixlo_f16 v2, v28, s2, 0
	ds_write_b16 v1, v2 offset:26400
	v_fma_mixlo_f16 v2, v13, s2, 0
	ds_write_b16 v1, v2 offset:10032
	v_fma_mixlo_f16 v2, v29, s2, 0
	ds_write_b16 v1, v2 offset:26928
	v_fma_mixlo_f16 v2, v14, s2, 0
	ds_write_b16 v1, v2 offset:12672
	v_fma_mixlo_f16 v2, v30, s2, 0
	ds_write_b16 v1, v2 offset:29568
	v_fma_mixlo_f16 v2, v15, s2, 0
	ds_write_b16 v1, v2 offset:13200
	v_fma_mixlo_f16 v2, v31, s2, 0
	ds_write_b16 v1, v2 offset:30096
	v_fma_mixlo_f16 v2, v16, s2, 0
	ds_write_b16 v1, v2 offset:13728
	v_fma_mixlo_f16 v2, v32, s2, 0
	ds_write_b16 v1, v2 offset:30624
	v_fma_mixlo_f16 v2, v17, s2, 0
	ds_write_b16 v1, v2 offset:14256
	v_fma_mixlo_f16 v2, v33, s2, 0
	ds_write_b16 v1, v2 offset:31152
	v_lshrrev_b32_e32 v1, 3, v0
	v_lshlrev_b32_e32 v0, 4, v0
	v_and_b32_e32 v4, 0x70, v0
	s_movk_i32 s2, 0x210
	v_mad_u32_u24 v12, v1, s2, v4
	s_ashr_i32 s2, s8, 31
	s_waitcnt lgkmcnt(0)
	s_barrier
	v_or_b32_e32 v6, s8, v1
	v_mov_b32_e32 v7, s2
	v_mov_b32_e32 v5, 0
	ds_read_b128 v[0:3], v12
	v_lshl_add_u64 v[4:5], s[16:17], 0, v[4:5]
	v_lshlrev_b64 v[6:7], 7, v[6:7]
	v_lshl_add_u64 v[8:9], v[4:5], 0, v[6:7]
	ds_read_b128 v[4:7], v12 offset:128
	s_mov_b32 s2, 0x200000
	s_waitcnt lgkmcnt(1)
	global_store_dwordx4 v[8:9], v[0:3], off
	s_nop 1
	v_add_co_u32_e32 v0, vcc, s2, v8
	s_nop 1
	v_addc_co_u32_e32 v1, vcc, 0, v9, vcc
	s_waitcnt lgkmcnt(0)
	global_store_dwordx4 v[0:1], v[4:7], off
	ds_read_b128 v[0:3], v12 offset:256
	ds_read_b128 v[4:7], v12 offset:384
	v_add_co_u32_e32 v10, vcc, 0x400000, v8
	s_nop 1
	v_addc_co_u32_e32 v11, vcc, 0, v9, vcc
	s_waitcnt lgkmcnt(1)
	global_store_dwordx4 v[10:11], v[0:3], off
	s_nop 1
	v_add_co_u32_e32 v0, vcc, 0x600000, v8
	s_nop 1
	v_addc_co_u32_e32 v1, vcc, 0, v9, vcc
	s_waitcnt lgkmcnt(0)
	global_store_dwordx4 v[0:1], v[4:7], off
	s_andn2_saveexec_b64 s[0:1], s[0:1]
	s_cbranch_execz .LBB1_234
.LBB1_248:
	v_and_b32_e32 v6, 31, v0
	v_bfe_u32 v7, v0, 5, 3
	s_cmp_lt_u32 s8, 0x2000
	s_cselect_b32 s50, s12, s14
	s_cselect_b32 s51, s13, s15
	s_and_b32 s0, s8, 0x1fff
	s_mul_i32 s1, s0, 0x2ee0
	s_add_u32 s50, s50, s1
	s_addc_u32 s51, s51, 0
	s_mov_b32 s52, s50
	s_mov_b32 s53, s51
	s_add_u32 s54, s50, 0x17700
	s_addc_u32 s55, s51, 0
	s_add_u32 s56, s50, 0x2ee00
	s_addc_u32 s57, s51, 0
	s_add_u32 s58, s50, 0x46500
	s_addc_u32 s59, s51, 0
	s_add_u32 s60, s50, 0x5dc00
	s_addc_u32 s61, s51, 0
	s_add_u32 s62, s50, 0x75300
	s_addc_u32 s63, s51, 0
	s_add_u32 s64, s50, 0x8ca00
	s_addc_u32 s65, s51, 0
	s_add_u32 s66, s50, 0xa4100
	s_addc_u32 s67, s51, 0
	v_and_b32_e32 v136, 3, v7
	v_lshl_add_u32 v137, v136, 1, v6
	s_movk_i32 s0, 0x2ee0
	v_mul_lo_u32 v2, v7, s0
	v_lshl_add_u32 v2, v137, 4, v2
	s_movk_i32 s0, 0x110
	v_mul_lo_u32 v3, v7, s0
	v_lshl_add_u32 v138, v137, 3, v3
	v_cmp_le_u32_e64 s[76:77], 32, v137
	v_cmp_gt_u32_e64 s[68:69], 14, v137
	s_not_b64 s[78:79], s[76:77]
	v_mov_b32_e32 v139, 0x0
	v_mov_b32_e32 v140, 0x4300
	v_cndmask_b32_e64 v139, v139, v140, s[76:77]
	v_add_u32_e32 v141, v138, v139
	v_mov_b32_e32 v139, 0x4400
	v_mov_b32_e32 v140, 0x8700
	v_cndmask_b32_e64 v139, v139, v140, s[76:77]
	v_add_u32_e32 v142, v138, v139
	v_mov_b32_e32 v139, 0x8800
	v_mov_b32_e32 v140, 0xcb00
	v_cndmask_b32_e64 v139, v139, v140, s[76:77]
	v_add_u32_e32 v143, v138, v139
	v_mov_b32_e32 v139, 0xcc00
	v_mov_b32_e32 v140, 0x10f00
	v_cndmask_b32_e64 v139, v139, v140, s[76:77]
	v_add_u32_e32 v144, v138, v139
	v_mov_b32_e32 v139, 0x11000
	v_mov_b32_e32 v140, 0xffffff00
	v_cndmask_b32_e64 v139, v139, v140, s[76:77]
	v_add_u32_e32 v145, v138, v139
	s_add_u32 s48, s18, 0x100000
	s_addc_u32 s49, s19, 0
	s_lshl_b32 s0, s10, 12
	v_add_u32_e32 v150, 0xfffffe00, v0
	v_lshl_add_u32 v150, v150, 4, s0
	global_load_dwordx4 v[152:155], v150, s[48:49]
	global_load_dwordx4 v[156:159], v150, s[18:19]
	v_mov_b32_e32 v104, 0
	v_mov_b32_e32 v105, 0
	v_mov_b32_e32 v106, 0
	v_mov_b32_e32 v107, 0
	s_mov_b64 s[70:71], exec
	s_mov_b64 exec, s[76:77]
	global_load_dwordx4 v[104:107], v2, s[52:53] offset:-512 sc1 nt
	s_mov_b64 exec, s[70:71]
	v_mov_b32_e32 v108, 0
	v_mov_b32_e32 v109, 0
	v_mov_b32_e32 v110, 0
	v_mov_b32_e32 v111, 0
	s_mov_b64 s[70:71], exec
	s_mov_b64 exec, s[76:77]
	global_load_dwordx4 v[108:111], v2, s[54:55] offset:-512 sc1 nt
	s_mov_b64 exec, s[70:71]
	v_mov_b32_e32 v112, 0
	v_mov_b32_e32 v113, 0
	v_mov_b32_e32 v114, 0
	v_mov_b32_e32 v115, 0
	s_mov_b64 s[70:71], exec
	s_mov_b64 exec, s[76:77]
	global_load_dwordx4 v[112:115], v2, s[56:57] offset:-512 sc1 nt
	s_mov_b64 exec, s[70:71]
	v_mov_b32_e32 v116, 0
	v_mov_b32_e32 v117, 0
	v_mov_b32_e32 v118, 0
	v_mov_b32_e32 v119, 0
	s_mov_b64 s[70:71], exec
	s_mov_b64 exec, s[76:77]
	global_load_dwordx4 v[116:119], v2, s[58:59] offset:-512 sc1 nt
	s_mov_b64 exec, s[70:71]
	v_mov_b32_e32 v120, 0
	v_mov_b32_e32 v121, 0
	v_mov_b32_e32 v122, 0
	v_mov_b32_e32 v123, 0
	s_mov_b64 s[70:71], exec
	s_mov_b64 exec, s[76:77]
	global_load_dwordx4 v[120:123], v2, s[60:61] offset:-512 sc1 nt
	s_mov_b64 exec, s[70:71]
	v_mov_b32_e32 v124, 0
	v_mov_b32_e32 v125, 0
	v_mov_b32_e32 v126, 0
	v_mov_b32_e32 v127, 0
	s_mov_b64 s[70:71], exec
	s_mov_b64 exec, s[76:77]
	global_load_dwordx4 v[124:127], v2, s[62:63] offset:-512 sc1 nt
	s_mov_b64 exec, s[70:71]
	v_mov_b32_e32 v128, 0
	v_mov_b32_e32 v129, 0
	v_mov_b32_e32 v130, 0
	v_mov_b32_e32 v131, 0
	s_mov_b64 s[70:71], exec
	s_mov_b64 exec, s[76:77]
	global_load_dwordx4 v[128:131], v2, s[64:65] offset:-512 sc1 nt
	s_mov_b64 exec, s[70:71]
	v_mov_b32_e32 v132, 0
	v_mov_b32_e32 v133, 0
	v_mov_b32_e32 v134, 0
	v_mov_b32_e32 v135, 0
	s_mov_b64 s[70:71], exec
	s_mov_b64 exec, s[76:77]
	global_load_dwordx4 v[132:135], v2, s[66:67] offset:-512 sc1 nt
	s_mov_b64 exec, s[70:71]
	global_load_dwordx4 v[8:11], v2, s[52:53] sc1 nt
	global_load_dwordx4 v[12:15], v2, s[54:55] sc1 nt
	global_load_dwordx4 v[16:19], v2, s[56:57] sc1 nt
	global_load_dwordx4 v[20:23], v2, s[58:59] sc1 nt
	global_load_dwordx4 v[24:27], v2, s[60:61] sc1 nt
	global_load_dwordx4 v[28:31], v2, s[62:63] sc1 nt
	global_load_dwordx4 v[32:35], v2, s[64:65] sc1 nt
	global_load_dwordx4 v[36:39], v2, s[66:67] sc1 nt
	global_load_dwordx4 v[40:43], v2, s[52:53] offset:512 sc1 nt
	global_load_dwordx4 v[44:47], v2, s[54:55] offset:512 sc1 nt
	global_load_dwordx4 v[48:51], v2, s[56:57] offset:512 sc1 nt
	global_load_dwordx4 v[52:55], v2, s[58:59] offset:512 sc1 nt
	global_load_dwordx4 v[56:59], v2, s[60:61] offset:512 sc1 nt
	global_load_dwordx4 v[60:63], v2, s[62:63] offset:512 sc1 nt
	global_load_dwordx4 v[64:67], v2, s[64:65] offset:512 sc1 nt
	global_load_dwordx4 v[68:71], v2, s[66:67] offset:512 sc1 nt
	global_load_dwordx4 v[72:75], v2, s[52:53] offset:1024 sc1 nt
	global_load_dwordx4 v[76:79], v2, s[54:55] offset:1024 sc1 nt
	global_load_dwordx4 v[80:83], v2, s[56:57] offset:1024 sc1 nt
	global_load_dwordx4 v[84:87], v2, s[58:59] offset:1024 sc1 nt
	global_load_dwordx4 v[88:91], v2, s[60:61] offset:1024 sc1 nt
	global_load_dwordx4 v[92:95], v2, s[62:63] offset:1024 sc1 nt
	global_load_dwordx4 v[96:99], v2, s[64:65] offset:1024 sc1 nt
	global_load_dwordx4 v[100:103], v2, s[66:67] offset:1024 sc1 nt
	s_waitcnt vmcnt(31)
	v_cvt_pk_f16_f32 v4, v104, v105
	v_cvt_pk_f16_f32 v5, v106, v107
	s_mov_b64 s[70:71], exec
	s_mov_b64 exec, s[76:77]
	ds_write_b64 v145, v[4:5]
	s_mov_b64 exec, s[70:71]
	global_load_dwordx4 v[104:107], v2, s[52:53] offset:1536 sc1 nt
	s_waitcnt vmcnt(31)
	v_cvt_pk_f16_f32 v4, v108, v109
	v_cvt_pk_f16_f32 v5, v110, v111
	s_mov_b64 s[70:71], exec
	s_mov_b64 exec, s[76:77]
	ds_write_b64 v145, v[4:5] offset:2176
	s_mov_b64 exec, s[70:71]
	global_load_dwordx4 v[108:111], v2, s[54:55] offset:1536 sc1 nt
	s_waitcnt vmcnt(31)
	v_cvt_pk_f16_f32 v4, v112, v113
	v_cvt_pk_f16_f32 v5, v114, v115
	s_mov_b64 s[70:71], exec
	s_mov_b64 exec, s[76:77]
	ds_write_b64 v145, v[4:5] offset:4352
	s_mov_b64 exec, s[70:71]
	global_load_dwordx4 v[112:115], v2, s[56:57] offset:1536 sc1 nt
	s_waitcnt vmcnt(31)
	v_cvt_pk_f16_f32 v4, v116, v117
	v_cvt_pk_f16_f32 v5, v118, v119
	s_mov_b64 s[70:71], exec
	s_mov_b64 exec, s[76:77]
	ds_write_b64 v145, v[4:5] offset:6528
	s_mov_b64 exec, s[70:71]
	global_load_dwordx4 v[116:119], v2, s[58:59] offset:1536 sc1 nt
	s_waitcnt vmcnt(31)
	v_cvt_pk_f16_f32 v4, v120, v121
	v_cvt_pk_f16_f32 v5, v122, v123
	s_mov_b64 s[70:71], exec
	s_mov_b64 exec, s[76:77]
	ds_write_b64 v145, v[4:5] offset:8704
	s_mov_b64 exec, s[70:71]
	global_load_dwordx4 v[120:123], v2, s[60:61] offset:1536 sc1 nt
	s_waitcnt vmcnt(31)
	v_cvt_pk_f16_f32 v4, v124, v125
	v_cvt_pk_f16_f32 v5, v126, v127
	s_mov_b64 s[70:71], exec
	s_mov_b64 exec, s[76:77]
	ds_write_b64 v145, v[4:5] offset:10880
	s_mov_b64 exec, s[70:71]
	global_load_dwordx4 v[124:127], v2, s[62:63] offset:1536 sc1 nt
	s_waitcnt vmcnt(31)
	v_cvt_pk_f16_f32 v4, v128, v129
	v_cvt_pk_f16_f32 v5, v130, v131
	s_mov_b64 s[70:71], exec
	s_mov_b64 exec, s[76:77]
	ds_write_b64 v145, v[4:5] offset:13056
	s_mov_b64 exec, s[70:71]
	global_load_dwordx4 v[128:131], v2, s[64:65] offset:1536 sc1 nt
	s_waitcnt vmcnt(31)
	v_cvt_pk_f16_f32 v4, v132, v133
	v_cvt_pk_f16_f32 v5, v134, v135
	s_mov_b64 s[70:71], exec
	s_mov_b64 exec, s[76:77]
	ds_write_b64 v145, v[4:5] offset:15232
	s_mov_b64 exec, s[70:71]
	global_load_dwordx4 v[132:135], v2, s[66:67] offset:1536 sc1 nt
	s_waitcnt vmcnt(40)
	v_mov_b32_e32 v151, 1
	v_lshlrev_b32_e32 v160, 2, v152
	v_lshlrev_b32_e32 v161, 2, v153
	v_lshlrev_b32_e32 v162, 2, v154
	v_lshlrev_b32_e32 v163, 2, v155
	global_atomic_add v164, v160, v151, s[20:21] sc0
	global_atomic_add v165, v161, v151, s[20:21] sc0
	global_atomic_add v166, v162, v151, s[20:21] sc0
	global_atomic_add v167, v163, v151, s[20:21] sc0
	s_waitcnt vmcnt(35)
	v_cvt_pk_f16_f32 v4, v8, v9
	v_cvt_pk_f16_f32 v5, v10, v11
	ds_write_b64 v141, v[4:5]
	s_waitcnt vmcnt(27)
	v_cvt_pk_f16_f32 v4, v40, v41
	v_cvt_pk_f16_f32 v5, v42, v43
	ds_write_b64 v142, v[4:5]
	global_load_dwordx4 v[8:11], v2, s[52:53] offset:2048 sc1 nt
	global_load_dwordx4 v[40:43], v2, s[52:53] offset:2560 sc1 nt
	s_waitcnt vmcnt(36)
	v_cvt_pk_f16_f32 v4, v12, v13
	v_cvt_pk_f16_f32 v5, v14, v15
	ds_write_b64 v141, v[4:5] offset:2176
	s_waitcnt vmcnt(28)
	v_cvt_pk_f16_f32 v4, v44, v45
	v_cvt_pk_f16_f32 v5, v46, v47
	ds_write_b64 v142, v[4:5] offset:2176
	global_load_dwordx4 v[12:15], v2, s[54:55] offset:2048 sc1 nt
	global_load_dwordx4 v[44:47], v2, s[54:55] offset:2560 sc1 nt
	s_waitcnt vmcnt(37)
	v_cvt_pk_f16_f32 v4, v16, v17
	v_cvt_pk_f16_f32 v5, v18, v19
	ds_write_b64 v141, v[4:5] offset:4352
	s_waitcnt vmcnt(29)
	v_cvt_pk_f16_f32 v4, v48, v49
	v_cvt_pk_f16_f32 v5, v50, v51
	ds_write_b64 v142, v[4:5] offset:4352
	global_load_dwordx4 v[16:19], v2, s[56:57] offset:2048 sc1 nt
	global_load_dwordx4 v[48:51], v2, s[56:57] offset:2560 sc1 nt
	s_waitcnt vmcnt(38)
	v_cvt_pk_f16_f32 v4, v20, v21
	v_cvt_pk_f16_f32 v5, v22, v23
	ds_write_b64 v141, v[4:5] offset:6528
	s_waitcnt vmcnt(30)
	v_cvt_pk_f16_f32 v4, v52, v53
	v_cvt_pk_f16_f32 v5, v54, v55
	ds_write_b64 v142, v[4:5] offset:6528
	global_load_dwordx4 v[20:23], v2, s[58:59] offset:2048 sc1 nt
	global_load_dwordx4 v[52:55], v2, s[58:59] offset:2560 sc1 nt
	s_waitcnt vmcnt(39)
	v_cvt_pk_f16_f32 v4, v24, v25
	v_cvt_pk_f16_f32 v5, v26, v27
	ds_write_b64 v141, v[4:5] offset:8704
	s_waitcnt vmcnt(31)
	v_cvt_pk_f16_f32 v4, v56, v57
	v_cvt_pk_f16_f32 v5, v58, v59
	ds_write_b64 v142, v[4:5] offset:8704
	global_load_dwordx4 v[24:27], v2, s[60:61] offset:2048 sc1 nt
	global_load_dwordx4 v[56:59], v2, s[60:61] offset:2560 sc1 nt
	s_waitcnt vmcnt(40)
	v_cvt_pk_f16_f32 v4, v28, v29
	v_cvt_pk_f16_f32 v5, v30, v31
	ds_write_b64 v141, v[4:5] offset:10880
	s_waitcnt vmcnt(32)
	v_cvt_pk_f16_f32 v4, v60, v61
	v_cvt_pk_f16_f32 v5, v62, v63
	ds_write_b64 v142, v[4:5] offset:10880
	global_load_dwordx4 v[28:31], v2, s[62:63] offset:2048 sc1 nt
	global_load_dwordx4 v[60:63], v2, s[62:63] offset:2560 sc1 nt
	s_waitcnt vmcnt(41)
	v_cvt_pk_f16_f32 v4, v32, v33
	v_cvt_pk_f16_f32 v5, v34, v35
	ds_write_b64 v141, v[4:5] offset:13056
	s_waitcnt vmcnt(33)
	v_cvt_pk_f16_f32 v4, v64, v65
	v_cvt_pk_f16_f32 v5, v66, v67
	ds_write_b64 v142, v[4:5] offset:13056
	global_load_dwordx4 v[32:35], v2, s[64:65] offset:2048 sc1 nt
	global_load_dwordx4 v[64:67], v2, s[64:65] offset:2560 sc1 nt
	s_waitcnt vmcnt(42)
	v_cvt_pk_f16_f32 v4, v36, v37
	v_cvt_pk_f16_f32 v5, v38, v39
	ds_write_b64 v141, v[4:5] offset:15232
	s_waitcnt vmcnt(34)
	v_cvt_pk_f16_f32 v4, v68, v69
	v_cvt_pk_f16_f32 v5, v70, v71
	ds_write_b64 v142, v[4:5] offset:15232
	global_load_dwordx4 v[36:39], v2, s[66:67] offset:2048 sc1 nt
	global_load_dwordx4 v[68:71], v2, s[66:67] offset:2560 sc1 nt
	s_waitcnt vmcnt(0)
	v_cmp_gt_i32_e32 vcc, 64, v164
	v_lshl_add_u32 v148, v152, 6, v164
	v_lshlrev_b32_e32 v148, 2, v148
	s_and_saveexec_b64 s[2:3], vcc
	global_store_dword v148, v156, s[22:23]
	s_xor_b64 exec, exec, s[2:3]
	s_cbranch_execz .Lg1_ld_ok_0
	v_mov_b32_e32 v149, 0x8000
	global_atomic_add v149, v149, v151, s[20:21] sc0
	s_waitcnt vmcnt(0)
	v_lshlrev_b32_e32 v149, 3, v149
	v_mov_b32_e32 v160, v152
	v_mov_b32_e32 v161, v156
	global_store_dwordx2 v149, v[160:161], s[28:29]

.Lg1_ld_ok_3:
	s_mov_b64 exec, -1
	s_waitcnt lgkmcnt(0)
	s_barrier
	s_waitcnt vmcnt(35)
	v_cvt_pk_f16_f32 v4, v72, v73
	v_cvt_pk_f16_f32 v5, v74, v75
	ds_write_b64 v143, v[4:5]
	s_waitcnt vmcnt(27)
	v_cvt_pk_f16_f32 v4, v104, v105
	v_cvt_pk_f16_f32 v5, v106, v107
	ds_write_b64 v144, v[4:5]
	global_load_dwordx4 v[72:75], v2, s[52:53] offset:3072 sc1 nt
	global_load_dwordx4 v[104:107], v2, s[52:53] offset:3584 sc1 nt
	s_waitcnt vmcnt(36)
	v_cvt_pk_f16_f32 v4, v76, v77
	v_cvt_pk_f16_f32 v5, v78, v79
	ds_write_b64 v143, v[4:5] offset:2176
	s_waitcnt vmcnt(28)
	v_cvt_pk_f16_f32 v4, v108, v109
	v_cvt_pk_f16_f32 v5, v110, v111
	ds_write_b64 v144, v[4:5] offset:2176
	global_load_dwordx4 v[76:79], v2, s[54:55] offset:3072 sc1 nt
	global_load_dwordx4 v[108:111], v2, s[54:55] offset:3584 sc1 nt
	s_waitcnt vmcnt(37)
	v_cvt_pk_f16_f32 v4, v80, v81
	v_cvt_pk_f16_f32 v5, v82, v83
	ds_write_b64 v143, v[4:5] offset:4352
	s_waitcnt vmcnt(29)
	v_cvt_pk_f16_f32 v4, v112, v113
	v_cvt_pk_f16_f32 v5, v114, v115
	ds_write_b64 v144, v[4:5] offset:4352
	global_load_dwordx4 v[80:83], v2, s[56:57] offset:3072 sc1 nt
	global_load_dwordx4 v[112:115], v2, s[56:57] offset:3584 sc1 nt
	s_waitcnt vmcnt(38)
	v_cvt_pk_f16_f32 v4, v84, v85
	v_cvt_pk_f16_f32 v5, v86, v87
	ds_write_b64 v143, v[4:5] offset:6528
	s_waitcnt vmcnt(30)
	v_cvt_pk_f16_f32 v4, v116, v117
	v_cvt_pk_f16_f32 v5, v118, v119
	ds_write_b64 v144, v[4:5] offset:6528
	global_load_dwordx4 v[84:87], v2, s[58:59] offset:3072 sc1 nt
	global_load_dwordx4 v[116:119], v2, s[58:59] offset:3584 sc1 nt
	s_waitcnt vmcnt(39)
	v_cvt_pk_f16_f32 v4, v88, v89
	v_cvt_pk_f16_f32 v5, v90, v91
	ds_write_b64 v143, v[4:5] offset:8704
	s_waitcnt vmcnt(31)
	v_cvt_pk_f16_f32 v4, v120, v121
	v_cvt_pk_f16_f32 v5, v122, v123
	ds_write_b64 v144, v[4:5] offset:8704
	global_load_dwordx4 v[88:91], v2, s[60:61] offset:3072 sc1 nt
	global_load_dwordx4 v[120:123], v2, s[60:61] offset:3584 sc1 nt
	s_waitcnt vmcnt(40)
	v_cvt_pk_f16_f32 v4, v92, v93
	v_cvt_pk_f16_f32 v5, v94, v95
	ds_write_b64 v143, v[4:5] offset:10880
	s_waitcnt vmcnt(32)
	v_cvt_pk_f16_f32 v4, v124, v125
	v_cvt_pk_f16_f32 v5, v126, v127
	ds_write_b64 v144, v[4:5] offset:10880
	global_load_dwordx4 v[92:95], v2, s[62:63] offset:3072 sc1 nt
	global_load_dwordx4 v[124:127], v2, s[62:63] offset:3584 sc1 nt
	s_waitcnt vmcnt(41)
	v_cvt_pk_f16_f32 v4, v96, v97
	v_cvt_pk_f16_f32 v5, v98, v99
	ds_write_b64 v143, v[4:5] offset:13056
	s_waitcnt vmcnt(33)
	v_cvt_pk_f16_f32 v4, v128, v129
	v_cvt_pk_f16_f32 v5, v130, v131
	ds_write_b64 v144, v[4:5] offset:13056
	global_load_dwordx4 v[96:99], v2, s[64:65] offset:3072 sc1 nt
	global_load_dwordx4 v[128:131], v2, s[64:65] offset:3584 sc1 nt
	s_waitcnt vmcnt(42)
	v_cvt_pk_f16_f32 v4, v100, v101
	v_cvt_pk_f16_f32 v5, v102, v103
	ds_write_b64 v143, v[4:5] offset:15232
	s_waitcnt vmcnt(34)
	v_cvt_pk_f16_f32 v4, v132, v133
	v_cvt_pk_f16_f32 v5, v134, v135
	ds_write_b64 v144, v[4:5] offset:15232
	global_load_dwordx4 v[100:103], v2, s[66:67] offset:3072 sc1 nt
	global_load_dwordx4 v[132:135], v2, s[66:67] offset:3584 sc1 nt
	s_waitcnt lgkmcnt(0)
	s_barrier
	s_waitcnt vmcnt(31)
	v_cvt_pk_f16_f32 v4, v8, v9
	v_cvt_pk_f16_f32 v5, v10, v11
	ds_write_b64 v145, v[4:5]
	s_waitcnt vmcnt(30)
	v_cvt_pk_f16_f32 v4, v40, v41
	v_cvt_pk_f16_f32 v5, v42, v43
	ds_write_b64 v141, v[4:5]
	v_add_u32_e32 v2, 0x1000, v2
	global_load_dwordx4 v[8:11], v2, s[52:53] sc1 nt
	global_load_dwordx4 v[40:43], v2, s[52:53] offset:512 sc1 nt
	s_waitcnt vmcnt(31)
	v_cvt_pk_f16_f32 v4, v12, v13
	v_cvt_pk_f16_f32 v5, v14, v15
	ds_write_b64 v145, v[4:5] offset:2176
	s_waitcnt vmcnt(30)
	v_cvt_pk_f16_f32 v4, v44, v45
	v_cvt_pk_f16_f32 v5, v46, v47
	ds_write_b64 v141, v[4:5] offset:2176
	global_load_dwordx4 v[12:15], v2, s[54:55] sc1 nt
	global_load_dwordx4 v[44:47], v2, s[54:55] offset:512 sc1 nt
	s_waitcnt vmcnt(31)
	v_cvt_pk_f16_f32 v4, v16, v17
	v_cvt_pk_f16_f32 v5, v18, v19
	ds_write_b64 v145, v[4:5] offset:4352
	s_waitcnt vmcnt(30)
	v_cvt_pk_f16_f32 v4, v48, v49
	v_cvt_pk_f16_f32 v5, v50, v51
	ds_write_b64 v141, v[4:5] offset:4352
	global_load_dwordx4 v[16:19], v2, s[56:57] sc1 nt
	global_load_dwordx4 v[48:51], v2, s[56:57] offset:512 sc1 nt
	s_waitcnt vmcnt(31)
	v_cvt_pk_f16_f32 v4, v20, v21
	v_cvt_pk_f16_f32 v5, v22, v23
	ds_write_b64 v145, v[4:5] offset:6528
	s_waitcnt vmcnt(30)
	v_cvt_pk_f16_f32 v4, v52, v53
	v_cvt_pk_f16_f32 v5, v54, v55
	ds_write_b64 v141, v[4:5] offset:6528
	global_load_dwordx4 v[20:23], v2, s[58:59] sc1 nt
	global_load_dwordx4 v[52:55], v2, s[58:59] offset:512 sc1 nt
	s_waitcnt vmcnt(31)
	v_cvt_pk_f16_f32 v4, v24, v25
	v_cvt_pk_f16_f32 v5, v26, v27
	ds_write_b64 v145, v[4:5] offset:8704
	s_waitcnt vmcnt(30)
	v_cvt_pk_f16_f32 v4, v56, v57
	v_cvt_pk_f16_f32 v5, v58, v59
	ds_write_b64 v141, v[4:5] offset:8704
	global_load_dwordx4 v[24:27], v2, s[60:61] sc1 nt
	global_load_dwordx4 v[56:59], v2, s[60:61] offset:512 sc1 nt
	s_waitcnt vmcnt(31)
	v_cvt_pk_f16_f32 v4, v28, v29
	v_cvt_pk_f16_f32 v5, v30, v31
	ds_write_b64 v145, v[4:5] offset:10880
	s_waitcnt vmcnt(30)
	v_cvt_pk_f16_f32 v4, v60, v61
	v_cvt_pk_f16_f32 v5, v62, v63
	ds_write_b64 v141, v[4:5] offset:10880
	global_load_dwordx4 v[28:31], v2, s[62:63] sc1 nt
	global_load_dwordx4 v[60:63], v2, s[62:63] offset:512 sc1 nt
	s_waitcnt vmcnt(31)
	v_cvt_pk_f16_f32 v4, v32, v33
	v_cvt_pk_f16_f32 v5, v34, v35
	ds_write_b64 v145, v[4:5] offset:13056
	s_waitcnt vmcnt(30)
	v_cvt_pk_f16_f32 v4, v64, v65
	v_cvt_pk_f16_f32 v5, v66, v67
	ds_write_b64 v141, v[4:5] offset:13056
	global_load_dwordx4 v[32:35], v2, s[64:65] sc1 nt
	global_load_dwordx4 v[64:67], v2, s[64:65] offset:512 sc1 nt
	s_waitcnt vmcnt(31)
	v_cvt_pk_f16_f32 v4, v36, v37
	v_cvt_pk_f16_f32 v5, v38, v39
	ds_write_b64 v145, v[4:5] offset:15232
	s_waitcnt vmcnt(30)
	v_cvt_pk_f16_f32 v4, v68, v69
	v_cvt_pk_f16_f32 v5, v70, v71
	ds_write_b64 v141, v[4:5] offset:15232
	global_load_dwordx4 v[36:39], v2, s[66:67] sc1 nt
	global_load_dwordx4 v[68:71], v2, s[66:67] offset:512 sc1 nt
	s_waitcnt lgkmcnt(0)
	s_barrier
	s_waitcnt vmcnt(31)
	v_cvt_pk_f16_f32 v4, v72, v73
	v_cvt_pk_f16_f32 v5, v74, v75
	ds_write_b64 v142, v[4:5]
	s_waitcnt vmcnt(30)
	v_cvt_pk_f16_f32 v4, v104, v105
	v_cvt_pk_f16_f32 v5, v106, v107
	ds_write_b64 v143, v[4:5]
	global_load_dwordx4 v[72:75], v2, s[52:53] offset:1024 sc1 nt
	global_load_dwordx4 v[104:107], v2, s[52:53] offset:1536 sc1 nt
	s_waitcnt vmcnt(31)
	v_cvt_pk_f16_f32 v4, v76, v77
	v_cvt_pk_f16_f32 v5, v78, v79
	ds_write_b64 v142, v[4:5] offset:2176
	s_waitcnt vmcnt(30)
	v_cvt_pk_f16_f32 v4, v108, v109
	v_cvt_pk_f16_f32 v5, v110, v111
	ds_write_b64 v143, v[4:5] offset:2176
	global_load_dwordx4 v[76:79], v2, s[54:55] offset:1024 sc1 nt
	global_load_dwordx4 v[108:111], v2, s[54:55] offset:1536 sc1 nt
	s_waitcnt vmcnt(31)
	v_cvt_pk_f16_f32 v4, v80, v81
	v_cvt_pk_f16_f32 v5, v82, v83
	ds_write_b64 v142, v[4:5] offset:4352
	s_waitcnt vmcnt(30)
	v_cvt_pk_f16_f32 v4, v112, v113
	v_cvt_pk_f16_f32 v5, v114, v115
	ds_write_b64 v143, v[4:5] offset:4352
	global_load_dwordx4 v[80:83], v2, s[56:57] offset:1024 sc1 nt
	global_load_dwordx4 v[112:115], v2, s[56:57] offset:1536 sc1 nt
	s_waitcnt vmcnt(31)
	v_cvt_pk_f16_f32 v4, v84, v85
	v_cvt_pk_f16_f32 v5, v86, v87
	ds_write_b64 v142, v[4:5] offset:6528
	s_waitcnt vmcnt(30)
	v_cvt_pk_f16_f32 v4, v116, v117
	v_cvt_pk_f16_f32 v5, v118, v119
	ds_write_b64 v143, v[4:5] offset:6528
	global_load_dwordx4 v[84:87], v2, s[58:59] offset:1024 sc1 nt
	global_load_dwordx4 v[116:119], v2, s[58:59] offset:1536 sc1 nt
	s_waitcnt vmcnt(31)
	v_cvt_pk_f16_f32 v4, v88, v89
	v_cvt_pk_f16_f32 v5, v90, v91
	ds_write_b64 v142, v[4:5] offset:8704
	s_waitcnt vmcnt(30)
	v_cvt_pk_f16_f32 v4, v120, v121
	v_cvt_pk_f16_f32 v5, v122, v123
	ds_write_b64 v143, v[4:5] offset:8704
	global_load_dwordx4 v[88:91], v2, s[60:61] offset:1024 sc1 nt
	global_load_dwordx4 v[120:123], v2, s[60:61] offset:1536 sc1 nt
	s_waitcnt vmcnt(31)
	v_cvt_pk_f16_f32 v4, v92, v93
	v_cvt_pk_f16_f32 v5, v94, v95
	ds_write_b64 v142, v[4:5] offset:10880
	s_waitcnt vmcnt(30)
	v_cvt_pk_f16_f32 v4, v124, v125
	v_cvt_pk_f16_f32 v5, v126, v127
	ds_write_b64 v143, v[4:5] offset:10880
	global_load_dwordx4 v[92:95], v2, s[62:63] offset:1024 sc1 nt
	global_load_dwordx4 v[124:127], v2, s[62:63] offset:1536 sc1 nt
	s_waitcnt vmcnt(31)
	v_cvt_pk_f16_f32 v4, v96, v97
	v_cvt_pk_f16_f32 v5, v98, v99
	ds_write_b64 v142, v[4:5] offset:13056
	s_waitcnt vmcnt(30)
	v_cvt_pk_f16_f32 v4, v128, v129
	v_cvt_pk_f16_f32 v5, v130, v131
	ds_write_b64 v143, v[4:5] offset:13056
	global_load_dwordx4 v[96:99], v2, s[64:65] offset:1024 sc1 nt
	global_load_dwordx4 v[128:131], v2, s[64:65] offset:1536 sc1 nt
	s_waitcnt vmcnt(31)
	v_cvt_pk_f16_f32 v4, v100, v101
	v_cvt_pk_f16_f32 v5, v102, v103
	ds_write_b64 v142, v[4:5] offset:15232
	s_waitcnt vmcnt(30)
	v_cvt_pk_f16_f32 v4, v132, v133
	v_cvt_pk_f16_f32 v5, v134, v135
	ds_write_b64 v143, v[4:5] offset:15232
	global_load_dwordx4 v[100:103], v2, s[66:67] offset:1024 sc1 nt
	global_load_dwordx4 v[132:135], v2, s[66:67] offset:1536 sc1 nt
	s_waitcnt lgkmcnt(0)
	s_barrier
	s_waitcnt vmcnt(31)
	v_cvt_pk_f16_f32 v4, v8, v9
	v_cvt_pk_f16_f32 v5, v10, v11
	ds_write_b64 v144, v[4:5]
	s_waitcnt vmcnt(30)
	v_cvt_pk_f16_f32 v4, v40, v41
	v_cvt_pk_f16_f32 v5, v42, v43
	ds_write_b64 v145, v[4:5]
	global_load_dwordx4 v[8:11], v2, s[52:53] offset:2048 sc1 nt
	global_load_dwordx4 v[40:43], v2, s[52:53] offset:2560 sc1 nt
	s_waitcnt vmcnt(31)
	v_cvt_pk_f16_f32 v4, v12, v13
	v_cvt_pk_f16_f32 v5, v14, v15
	ds_write_b64 v144, v[4:5] offset:2176
	s_waitcnt vmcnt(30)
	v_cvt_pk_f16_f32 v4, v44, v45
	v_cvt_pk_f16_f32 v5, v46, v47
	ds_write_b64 v145, v[4:5] offset:2176
	global_load_dwordx4 v[12:15], v2, s[54:55] offset:2048 sc1 nt
	global_load_dwordx4 v[44:47], v2, s[54:55] offset:2560 sc1 nt
	s_waitcnt vmcnt(31)
	v_cvt_pk_f16_f32 v4, v16, v17
	v_cvt_pk_f16_f32 v5, v18, v19
	ds_write_b64 v144, v[4:5] offset:4352
	s_waitcnt vmcnt(30)
	v_cvt_pk_f16_f32 v4, v48, v49
	v_cvt_pk_f16_f32 v5, v50, v51
	ds_write_b64 v145, v[4:5] offset:4352
	global_load_dwordx4 v[16:19], v2, s[56:57] offset:2048 sc1 nt
	global_load_dwordx4 v[48:51], v2, s[56:57] offset:2560 sc1 nt
	s_waitcnt vmcnt(31)
	v_cvt_pk_f16_f32 v4, v20, v21
	v_cvt_pk_f16_f32 v5, v22, v23
	ds_write_b64 v144, v[4:5] offset:6528
	s_waitcnt vmcnt(30)
	v_cvt_pk_f16_f32 v4, v52, v53
	v_cvt_pk_f16_f32 v5, v54, v55
	ds_write_b64 v145, v[4:5] offset:6528
	global_load_dwordx4 v[20:23], v2, s[58:59] offset:2048 sc1 nt
	global_load_dwordx4 v[52:55], v2, s[58:59] offset:2560 sc1 nt
	s_waitcnt vmcnt(31)
	v_cvt_pk_f16_f32 v4, v24, v25
	v_cvt_pk_f16_f32 v5, v26, v27
	ds_write_b64 v144, v[4:5] offset:8704
	s_waitcnt vmcnt(30)
	v_cvt_pk_f16_f32 v4, v56, v57
	v_cvt_pk_f16_f32 v5, v58, v59
	ds_write_b64 v145, v[4:5] offset:8704
	global_load_dwordx4 v[24:27], v2, s[60:61] offset:2048 sc1 nt
	global_load_dwordx4 v[56:59], v2, s[60:61] offset:2560 sc1 nt
	s_waitcnt vmcnt(31)
	v_cvt_pk_f16_f32 v4, v28, v29
	v_cvt_pk_f16_f32 v5, v30, v31
	ds_write_b64 v144, v[4:5] offset:10880
	s_waitcnt vmcnt(30)
	v_cvt_pk_f16_f32 v4, v60, v61
	v_cvt_pk_f16_f32 v5, v62, v63
	ds_write_b64 v145, v[4:5] offset:10880
	global_load_dwordx4 v[28:31], v2, s[62:63] offset:2048 sc1 nt
	global_load_dwordx4 v[60:63], v2, s[62:63] offset:2560 sc1 nt
	s_waitcnt vmcnt(31)
	v_cvt_pk_f16_f32 v4, v32, v33
	v_cvt_pk_f16_f32 v5, v34, v35
	ds_write_b64 v144, v[4:5] offset:13056
	s_waitcnt vmcnt(30)
	v_cvt_pk_f16_f32 v4, v64, v65
	v_cvt_pk_f16_f32 v5, v66, v67
	ds_write_b64 v145, v[4:5] offset:13056
	global_load_dwordx4 v[32:35], v2, s[64:65] offset:2048 sc1 nt
	global_load_dwordx4 v[64:67], v2, s[64:65] offset:2560 sc1 nt
	s_waitcnt vmcnt(31)
	v_cvt_pk_f16_f32 v4, v36, v37
	v_cvt_pk_f16_f32 v5, v38, v39
	ds_write_b64 v144, v[4:5] offset:15232
	s_waitcnt vmcnt(30)
	v_cvt_pk_f16_f32 v4, v68, v69
	v_cvt_pk_f16_f32 v5, v70, v71
	ds_write_b64 v145, v[4:5] offset:15232
	global_load_dwordx4 v[36:39], v2, s[66:67] offset:2048 sc1 nt
	global_load_dwordx4 v[68:71], v2, s[66:67] offset:2560 sc1 nt
	s_waitcnt lgkmcnt(0)
	s_barrier
	s_waitcnt vmcnt(31)
	v_cvt_pk_f16_f32 v4, v72, v73
	v_cvt_pk_f16_f32 v5, v74, v75
	ds_write_b64 v141, v[4:5]
	s_waitcnt vmcnt(30)
	v_cvt_pk_f16_f32 v4, v104, v105
	v_cvt_pk_f16_f32 v5, v106, v107
	ds_write_b64 v142, v[4:5]
	global_load_dwordx4 v[72:75], v2, s[52:53] offset:3072 sc1 nt
	global_load_dwordx4 v[104:107], v2, s[52:53] offset:3584 sc1 nt
	s_waitcnt vmcnt(31)
	v_cvt_pk_f16_f32 v4, v76, v77
	v_cvt_pk_f16_f32 v5, v78, v79
	ds_write_b64 v141, v[4:5] offset:2176
	s_waitcnt vmcnt(30)
	v_cvt_pk_f16_f32 v4, v108, v109
	v_cvt_pk_f16_f32 v5, v110, v111
	ds_write_b64 v142, v[4:5] offset:2176
	global_load_dwordx4 v[76:79], v2, s[54:55] offset:3072 sc1 nt
	global_load_dwordx4 v[108:111], v2, s[54:55] offset:3584 sc1 nt
	s_waitcnt vmcnt(31)
	v_cvt_pk_f16_f32 v4, v80, v81
	v_cvt_pk_f16_f32 v5, v82, v83
	ds_write_b64 v141, v[4:5] offset:4352
	s_waitcnt vmcnt(30)
	v_cvt_pk_f16_f32 v4, v112, v113
	v_cvt_pk_f16_f32 v5, v114, v115
	ds_write_b64 v142, v[4:5] offset:4352
	global_load_dwordx4 v[80:83], v2, s[56:57] offset:3072 sc1 nt
	global_load_dwordx4 v[112:115], v2, s[56:57] offset:3584 sc1 nt
	s_waitcnt vmcnt(31)
	v_cvt_pk_f16_f32 v4, v84, v85
	v_cvt_pk_f16_f32 v5, v86, v87
	ds_write_b64 v141, v[4:5] offset:6528
	s_waitcnt vmcnt(30)
	v_cvt_pk_f16_f32 v4, v116, v117
	v_cvt_pk_f16_f32 v5, v118, v119
	ds_write_b64 v142, v[4:5] offset:6528
	global_load_dwordx4 v[84:87], v2, s[58:59] offset:3072 sc1 nt
	global_load_dwordx4 v[116:119], v2, s[58:59] offset:3584 sc1 nt
	s_waitcnt vmcnt(31)
	v_cvt_pk_f16_f32 v4, v88, v89
	v_cvt_pk_f16_f32 v5, v90, v91
	ds_write_b64 v141, v[4:5] offset:8704
	s_waitcnt vmcnt(30)
	v_cvt_pk_f16_f32 v4, v120, v121
	v_cvt_pk_f16_f32 v5, v122, v123
	ds_write_b64 v142, v[4:5] offset:8704
	global_load_dwordx4 v[88:91], v2, s[60:61] offset:3072 sc1 nt
	global_load_dwordx4 v[120:123], v2, s[60:61] offset:3584 sc1 nt
	s_waitcnt vmcnt(31)
	v_cvt_pk_f16_f32 v4, v92, v93
	v_cvt_pk_f16_f32 v5, v94, v95
	ds_write_b64 v141, v[4:5] offset:10880
	s_waitcnt vmcnt(30)
	v_cvt_pk_f16_f32 v4, v124, v125
	v_cvt_pk_f16_f32 v5, v126, v127
	ds_write_b64 v142, v[4:5] offset:10880
	global_load_dwordx4 v[92:95], v2, s[62:63] offset:3072 sc1 nt
	global_load_dwordx4 v[124:127], v2, s[62:63] offset:3584 sc1 nt
	s_waitcnt vmcnt(31)
	v_cvt_pk_f16_f32 v4, v96, v97
	v_cvt_pk_f16_f32 v5, v98, v99
	ds_write_b64 v141, v[4:5] offset:13056
	s_waitcnt vmcnt(30)
	v_cvt_pk_f16_f32 v4, v128, v129
	v_cvt_pk_f16_f32 v5, v130, v131
	ds_write_b64 v142, v[4:5] offset:13056
	global_load_dwordx4 v[96:99], v2, s[64:65] offset:3072 sc1 nt
	global_load_dwordx4 v[128:131], v2, s[64:65] offset:3584 sc1 nt
	s_waitcnt vmcnt(31)
	v_cvt_pk_f16_f32 v4, v100, v101
	v_cvt_pk_f16_f32 v5, v102, v103
	ds_write_b64 v141, v[4:5] offset:15232
	s_waitcnt vmcnt(30)
	v_cvt_pk_f16_f32 v4, v132, v133
	v_cvt_pk_f16_f32 v5, v134, v135
	ds_write_b64 v142, v[4:5] offset:15232
	global_load_dwordx4 v[100:103], v2, s[66:67] offset:3072 sc1 nt
	global_load_dwordx4 v[132:135], v2, s[66:67] offset:3584 sc1 nt
	s_waitcnt lgkmcnt(0)
	s_barrier
	s_waitcnt vmcnt(31)
	v_cvt_pk_f16_f32 v4, v8, v9
	v_cvt_pk_f16_f32 v5, v10, v11
	ds_write_b64 v143, v[4:5]
	s_waitcnt vmcnt(30)
	v_cvt_pk_f16_f32 v4, v40, v41
	v_cvt_pk_f16_f32 v5, v42, v43
	ds_write_b64 v144, v[4:5]
	v_add_u32_e32 v2, 0x1000, v2
	global_load_dwordx4 v[8:11], v2, s[52:53] sc1 nt
	global_load_dwordx4 v[40:43], v2, s[52:53] offset:512 sc1 nt
	s_waitcnt vmcnt(31)
	v_cvt_pk_f16_f32 v4, v12, v13
	v_cvt_pk_f16_f32 v5, v14, v15
	ds_write_b64 v143, v[4:5] offset:2176
	s_waitcnt vmcnt(30)
	v_cvt_pk_f16_f32 v4, v44, v45
	v_cvt_pk_f16_f32 v5, v46, v47
	ds_write_b64 v144, v[4:5] offset:2176
	global_load_dwordx4 v[12:15], v2, s[54:55] sc1 nt
	global_load_dwordx4 v[44:47], v2, s[54:55] offset:512 sc1 nt
	s_waitcnt vmcnt(31)
	v_cvt_pk_f16_f32 v4, v16, v17
	v_cvt_pk_f16_f32 v5, v18, v19
	ds_write_b64 v143, v[4:5] offset:4352
	s_waitcnt vmcnt(30)
	v_cvt_pk_f16_f32 v4, v48, v49
	v_cvt_pk_f16_f32 v5, v50, v51
	ds_write_b64 v144, v[4:5] offset:4352
	global_load_dwordx4 v[16:19], v2, s[56:57] sc1 nt
	global_load_dwordx4 v[48:51], v2, s[56:57] offset:512 sc1 nt
	s_waitcnt vmcnt(31)
	v_cvt_pk_f16_f32 v4, v20, v21
	v_cvt_pk_f16_f32 v5, v22, v23
	ds_write_b64 v143, v[4:5] offset:6528
	s_waitcnt vmcnt(30)
	v_cvt_pk_f16_f32 v4, v52, v53
	v_cvt_pk_f16_f32 v5, v54, v55
	ds_write_b64 v144, v[4:5] offset:6528
	global_load_dwordx4 v[20:23], v2, s[58:59] sc1 nt
	global_load_dwordx4 v[52:55], v2, s[58:59] offset:512 sc1 nt
	s_waitcnt vmcnt(31)
	v_cvt_pk_f16_f32 v4, v24, v25
	v_cvt_pk_f16_f32 v5, v26, v27
	ds_write_b64 v143, v[4:5] offset:8704
	s_waitcnt vmcnt(30)
	v_cvt_pk_f16_f32 v4, v56, v57
	v_cvt_pk_f16_f32 v5, v58, v59
	ds_write_b64 v144, v[4:5] offset:8704
	global_load_dwordx4 v[24:27], v2, s[60:61] sc1 nt
	global_load_dwordx4 v[56:59], v2, s[60:61] offset:512 sc1 nt
	s_waitcnt vmcnt(31)
	v_cvt_pk_f16_f32 v4, v28, v29
	v_cvt_pk_f16_f32 v5, v30, v31
	ds_write_b64 v143, v[4:5] offset:10880
	s_waitcnt vmcnt(30)
	v_cvt_pk_f16_f32 v4, v60, v61
	v_cvt_pk_f16_f32 v5, v62, v63
	ds_write_b64 v144, v[4:5] offset:10880
	global_load_dwordx4 v[28:31], v2, s[62:63] sc1 nt
	global_load_dwordx4 v[60:63], v2, s[62:63] offset:512 sc1 nt
	s_waitcnt vmcnt(31)
	v_cvt_pk_f16_f32 v4, v32, v33
	v_cvt_pk_f16_f32 v5, v34, v35
	ds_write_b64 v143, v[4:5] offset:13056
	s_waitcnt vmcnt(30)
	v_cvt_pk_f16_f32 v4, v64, v65
	v_cvt_pk_f16_f32 v5, v66, v67
	ds_write_b64 v144, v[4:5] offset:13056
	global_load_dwordx4 v[32:35], v2, s[64:65] sc1 nt
	global_load_dwordx4 v[64:67], v2, s[64:65] offset:512 sc1 nt
	s_waitcnt vmcnt(31)
	v_cvt_pk_f16_f32 v4, v36, v37
	v_cvt_pk_f16_f32 v5, v38, v39
	ds_write_b64 v143, v[4:5] offset:15232
	s_waitcnt vmcnt(30)
	v_cvt_pk_f16_f32 v4, v68, v69
	v_cvt_pk_f16_f32 v5, v70, v71
	ds_write_b64 v144, v[4:5] offset:15232
	global_load_dwordx4 v[36:39], v2, s[66:67] sc1 nt
	global_load_dwordx4 v[68:71], v2, s[66:67] offset:512 sc1 nt
	s_waitcnt lgkmcnt(0)
	s_barrier
	s_waitcnt vmcnt(31)
	v_cvt_pk_f16_f32 v4, v72, v73
	v_cvt_pk_f16_f32 v5, v74, v75
	ds_write_b64 v145, v[4:5]
	s_waitcnt vmcnt(30)
	v_cvt_pk_f16_f32 v4, v104, v105
	v_cvt_pk_f16_f32 v5, v106, v107
	ds_write_b64 v141, v[4:5]
	global_load_dwordx4 v[72:75], v2, s[52:53] offset:1024 sc1 nt
	global_load_dwordx4 v[104:107], v2, s[52:53] offset:1536 sc1 nt
	s_waitcnt vmcnt(31)
	v_cvt_pk_f16_f32 v4, v76, v77
	v_cvt_pk_f16_f32 v5, v78, v79
	ds_write_b64 v145, v[4:5] offset:2176
	s_waitcnt vmcnt(30)
	v_cvt_pk_f16_f32 v4, v108, v109
	v_cvt_pk_f16_f32 v5, v110, v111
	ds_write_b64 v141, v[4:5] offset:2176
	global_load_dwordx4 v[76:79], v2, s[54:55] offset:1024 sc1 nt
	global_load_dwordx4 v[108:111], v2, s[54:55] offset:1536 sc1 nt
	s_waitcnt vmcnt(31)
	v_cvt_pk_f16_f32 v4, v80, v81
	v_cvt_pk_f16_f32 v5, v82, v83
	ds_write_b64 v145, v[4:5] offset:4352
	s_waitcnt vmcnt(30)
	v_cvt_pk_f16_f32 v4, v112, v113
	v_cvt_pk_f16_f32 v5, v114, v115
	ds_write_b64 v141, v[4:5] offset:4352
	global_load_dwordx4 v[80:83], v2, s[56:57] offset:1024 sc1 nt
	global_load_dwordx4 v[112:115], v2, s[56:57] offset:1536 sc1 nt
	s_waitcnt vmcnt(31)
	v_cvt_pk_f16_f32 v4, v84, v85
	v_cvt_pk_f16_f32 v5, v86, v87
	ds_write_b64 v145, v[4:5] offset:6528
	s_waitcnt vmcnt(30)
	v_cvt_pk_f16_f32 v4, v116, v117
	v_cvt_pk_f16_f32 v5, v118, v119
	ds_write_b64 v141, v[4:5] offset:6528
	global_load_dwordx4 v[84:87], v2, s[58:59] offset:1024 sc1 nt
	global_load_dwordx4 v[116:119], v2, s[58:59] offset:1536 sc1 nt
	s_waitcnt vmcnt(31)
	v_cvt_pk_f16_f32 v4, v88, v89
	v_cvt_pk_f16_f32 v5, v90, v91
	ds_write_b64 v145, v[4:5] offset:8704
	s_waitcnt vmcnt(30)
	v_cvt_pk_f16_f32 v4, v120, v121
	v_cvt_pk_f16_f32 v5, v122, v123
	ds_write_b64 v141, v[4:5] offset:8704
	global_load_dwordx4 v[88:91], v2, s[60:61] offset:1024 sc1 nt
	global_load_dwordx4 v[120:123], v2, s[60:61] offset:1536 sc1 nt
	s_waitcnt vmcnt(31)
	v_cvt_pk_f16_f32 v4, v92, v93
	v_cvt_pk_f16_f32 v5, v94, v95
	ds_write_b64 v145, v[4:5] offset:10880
	s_waitcnt vmcnt(30)
	v_cvt_pk_f16_f32 v4, v124, v125
	v_cvt_pk_f16_f32 v5, v126, v127
	ds_write_b64 v141, v[4:5] offset:10880
	global_load_dwordx4 v[92:95], v2, s[62:63] offset:1024 sc1 nt
	global_load_dwordx4 v[124:127], v2, s[62:63] offset:1536 sc1 nt
	s_waitcnt vmcnt(31)
	v_cvt_pk_f16_f32 v4, v96, v97
	v_cvt_pk_f16_f32 v5, v98, v99
	ds_write_b64 v145, v[4:5] offset:13056
	s_waitcnt vmcnt(30)
	v_cvt_pk_f16_f32 v4, v128, v129
	v_cvt_pk_f16_f32 v5, v130, v131
	ds_write_b64 v141, v[4:5] offset:13056
	global_load_dwordx4 v[96:99], v2, s[64:65] offset:1024 sc1 nt
	global_load_dwordx4 v[128:131], v2, s[64:65] offset:1536 sc1 nt
	s_waitcnt vmcnt(31)
	v_cvt_pk_f16_f32 v4, v100, v101
	v_cvt_pk_f16_f32 v5, v102, v103
	ds_write_b64 v145, v[4:5] offset:15232
	s_waitcnt vmcnt(30)
	v_cvt_pk_f16_f32 v4, v132, v133
	v_cvt_pk_f16_f32 v5, v134, v135
	ds_write_b64 v141, v[4:5] offset:15232
	global_load_dwordx4 v[100:103], v2, s[66:67] offset:1024 sc1 nt
	global_load_dwordx4 v[132:135], v2, s[66:67] offset:1536 sc1 nt
	s_waitcnt lgkmcnt(0)
	s_barrier
	s_waitcnt vmcnt(31)
	v_cvt_pk_f16_f32 v4, v8, v9
	v_cvt_pk_f16_f32 v5, v10, v11
	ds_write_b64 v142, v[4:5]
	s_waitcnt vmcnt(30)
	v_cvt_pk_f16_f32 v4, v40, v41
	v_cvt_pk_f16_f32 v5, v42, v43
	ds_write_b64 v143, v[4:5]
	global_load_dwordx4 v[8:11], v2, s[52:53] offset:2048 sc1 nt
	global_load_dwordx4 v[40:43], v2, s[52:53] offset:2560 sc1 nt
	s_waitcnt vmcnt(31)
	v_cvt_pk_f16_f32 v4, v12, v13
	v_cvt_pk_f16_f32 v5, v14, v15
	ds_write_b64 v142, v[4:5] offset:2176
	s_waitcnt vmcnt(30)
	v_cvt_pk_f16_f32 v4, v44, v45
	v_cvt_pk_f16_f32 v5, v46, v47
	ds_write_b64 v143, v[4:5] offset:2176
	global_load_dwordx4 v[12:15], v2, s[54:55] offset:2048 sc1 nt
	global_load_dwordx4 v[44:47], v2, s[54:55] offset:2560 sc1 nt
	s_waitcnt vmcnt(31)
	v_cvt_pk_f16_f32 v4, v16, v17
	v_cvt_pk_f16_f32 v5, v18, v19
	ds_write_b64 v142, v[4:5] offset:4352
	s_waitcnt vmcnt(30)
	v_cvt_pk_f16_f32 v4, v48, v49
	v_cvt_pk_f16_f32 v5, v50, v51
	ds_write_b64 v143, v[4:5] offset:4352
	global_load_dwordx4 v[16:19], v2, s[56:57] offset:2048 sc1 nt
	global_load_dwordx4 v[48:51], v2, s[56:57] offset:2560 sc1 nt
	s_waitcnt vmcnt(31)
	v_cvt_pk_f16_f32 v4, v20, v21
	v_cvt_pk_f16_f32 v5, v22, v23
	ds_write_b64 v142, v[4:5] offset:6528
	s_waitcnt vmcnt(30)
	v_cvt_pk_f16_f32 v4, v52, v53
	v_cvt_pk_f16_f32 v5, v54, v55
	ds_write_b64 v143, v[4:5] offset:6528
	global_load_dwordx4 v[20:23], v2, s[58:59] offset:2048 sc1 nt
	global_load_dwordx4 v[52:55], v2, s[58:59] offset:2560 sc1 nt
	s_waitcnt vmcnt(31)
	v_cvt_pk_f16_f32 v4, v24, v25
	v_cvt_pk_f16_f32 v5, v26, v27
	ds_write_b64 v142, v[4:5] offset:8704
	s_waitcnt vmcnt(30)
	v_cvt_pk_f16_f32 v4, v56, v57
	v_cvt_pk_f16_f32 v5, v58, v59
	ds_write_b64 v143, v[4:5] offset:8704
	global_load_dwordx4 v[24:27], v2, s[60:61] offset:2048 sc1 nt
	global_load_dwordx4 v[56:59], v2, s[60:61] offset:2560 sc1 nt
	s_waitcnt vmcnt(31)
	v_cvt_pk_f16_f32 v4, v28, v29
	v_cvt_pk_f16_f32 v5, v30, v31
	ds_write_b64 v142, v[4:5] offset:10880
	s_waitcnt vmcnt(30)
	v_cvt_pk_f16_f32 v4, v60, v61
	v_cvt_pk_f16_f32 v5, v62, v63
	ds_write_b64 v143, v[4:5] offset:10880
	global_load_dwordx4 v[28:31], v2, s[62:63] offset:2048 sc1 nt
	global_load_dwordx4 v[60:63], v2, s[62:63] offset:2560 sc1 nt
	s_waitcnt vmcnt(31)
	v_cvt_pk_f16_f32 v4, v32, v33
	v_cvt_pk_f16_f32 v5, v34, v35
	ds_write_b64 v142, v[4:5] offset:13056
	s_waitcnt vmcnt(30)
	v_cvt_pk_f16_f32 v4, v64, v65
	v_cvt_pk_f16_f32 v5, v66, v67
	ds_write_b64 v143, v[4:5] offset:13056
	global_load_dwordx4 v[32:35], v2, s[64:65] offset:2048 sc1 nt
	global_load_dwordx4 v[64:67], v2, s[64:65] offset:2560 sc1 nt
	s_waitcnt vmcnt(31)
	v_cvt_pk_f16_f32 v4, v36, v37
	v_cvt_pk_f16_f32 v5, v38, v39
	ds_write_b64 v142, v[4:5] offset:15232
	s_waitcnt vmcnt(30)
	v_cvt_pk_f16_f32 v4, v68, v69
	v_cvt_pk_f16_f32 v5, v70, v71
	ds_write_b64 v143, v[4:5] offset:15232
	global_load_dwordx4 v[36:39], v2, s[66:67] offset:2048 sc1 nt
	global_load_dwordx4 v[68:71], v2, s[66:67] offset:2560 sc1 nt
	s_waitcnt lgkmcnt(0)
	s_barrier
	s_waitcnt vmcnt(31)
	v_cvt_pk_f16_f32 v4, v72, v73
	v_cvt_pk_f16_f32 v5, v74, v75
	ds_write_b64 v144, v[4:5]
	s_waitcnt vmcnt(30)
	v_cvt_pk_f16_f32 v4, v104, v105
	v_cvt_pk_f16_f32 v5, v106, v107
	ds_write_b64 v145, v[4:5]
	global_load_dwordx4 v[72:75], v2, s[52:53] offset:3072 sc1 nt
	v_mov_b32_e32 v104, 0
	v_mov_b32_e32 v105, 0
	v_mov_b32_e32 v106, 0
	v_mov_b32_e32 v107, 0
	s_mov_b64 s[70:71], exec
	s_mov_b64 exec, s[68:69]
	global_load_dwordx4 v[104:107], v2, s[52:53] offset:3584 sc1 nt
	s_mov_b64 exec, s[70:71]
	s_waitcnt vmcnt(31)
	v_cvt_pk_f16_f32 v4, v76, v77
	v_cvt_pk_f16_f32 v5, v78, v79
	ds_write_b64 v144, v[4:5] offset:2176
	s_waitcnt vmcnt(30)
	v_cvt_pk_f16_f32 v4, v108, v109
	v_cvt_pk_f16_f32 v5, v110, v111
	ds_write_b64 v145, v[4:5] offset:2176
	global_load_dwordx4 v[76:79], v2, s[54:55] offset:3072 sc1 nt
	v_mov_b32_e32 v108, 0
	v_mov_b32_e32 v109, 0
	v_mov_b32_e32 v110, 0
	v_mov_b32_e32 v111, 0
	s_mov_b64 s[70:71], exec
	s_mov_b64 exec, s[68:69]
	global_load_dwordx4 v[108:111], v2, s[54:55] offset:3584 sc1 nt
	s_mov_b64 exec, s[70:71]
	s_waitcnt vmcnt(31)
	v_cvt_pk_f16_f32 v4, v80, v81
	v_cvt_pk_f16_f32 v5, v82, v83
	ds_write_b64 v144, v[4:5] offset:4352
	s_waitcnt vmcnt(30)
	v_cvt_pk_f16_f32 v4, v112, v113
	v_cvt_pk_f16_f32 v5, v114, v115
	ds_write_b64 v145, v[4:5] offset:4352
	global_load_dwordx4 v[80:83], v2, s[56:57] offset:3072 sc1 nt
	v_mov_b32_e32 v112, 0
	v_mov_b32_e32 v113, 0
	v_mov_b32_e32 v114, 0
	v_mov_b32_e32 v115, 0
	s_mov_b64 s[70:71], exec
	s_mov_b64 exec, s[68:69]
	global_load_dwordx4 v[112:115], v2, s[56:57] offset:3584 sc1 nt
	s_mov_b64 exec, s[70:71]
	s_waitcnt vmcnt(31)
	v_cvt_pk_f16_f32 v4, v84, v85
	v_cvt_pk_f16_f32 v5, v86, v87
	ds_write_b64 v144, v[4:5] offset:6528
	s_waitcnt vmcnt(30)
	v_cvt_pk_f16_f32 v4, v116, v117
	v_cvt_pk_f16_f32 v5, v118, v119
	ds_write_b64 v145, v[4:5] offset:6528
	global_load_dwordx4 v[84:87], v2, s[58:59] offset:3072 sc1 nt
	v_mov_b32_e32 v116, 0
	v_mov_b32_e32 v117, 0
	v_mov_b32_e32 v118, 0
	v_mov_b32_e32 v119, 0
	s_mov_b64 s[70:71], exec
	s_mov_b64 exec, s[68:69]
	global_load_dwordx4 v[116:119], v2, s[58:59] offset:3584 sc1 nt
	s_mov_b64 exec, s[70:71]
	s_waitcnt vmcnt(31)
	v_cvt_pk_f16_f32 v4, v88, v89
	v_cvt_pk_f16_f32 v5, v90, v91
	ds_write_b64 v144, v[4:5] offset:8704
	s_waitcnt vmcnt(30)
	v_cvt_pk_f16_f32 v4, v120, v121
	v_cvt_pk_f16_f32 v5, v122, v123
	ds_write_b64 v145, v[4:5] offset:8704
	global_load_dwordx4 v[88:91], v2, s[60:61] offset:3072 sc1 nt
	v_mov_b32_e32 v120, 0
	v_mov_b32_e32 v121, 0
	v_mov_b32_e32 v122, 0
	v_mov_b32_e32 v123, 0
	s_mov_b64 s[70:71], exec
	s_mov_b64 exec, s[68:69]
	global_load_dwordx4 v[120:123], v2, s[60:61] offset:3584 sc1 nt
	s_mov_b64 exec, s[70:71]
	s_waitcnt vmcnt(31)
	v_cvt_pk_f16_f32 v4, v92, v93
	v_cvt_pk_f16_f32 v5, v94, v95
	ds_write_b64 v144, v[4:5] offset:10880
	s_waitcnt vmcnt(30)
	v_cvt_pk_f16_f32 v4, v124, v125
	v_cvt_pk_f16_f32 v5, v126, v127
	ds_write_b64 v145, v[4:5] offset:10880
	global_load_dwordx4 v[92:95], v2, s[62:63] offset:3072 sc1 nt
	v_mov_b32_e32 v124, 0
	v_mov_b32_e32 v125, 0
	v_mov_b32_e32 v126, 0
	v_mov_b32_e32 v127, 0
	s_mov_b64 s[70:71], exec
	s_mov_b64 exec, s[68:69]
	global_load_dwordx4 v[124:127], v2, s[62:63] offset:3584 sc1 nt
	s_mov_b64 exec, s[70:71]
	s_waitcnt vmcnt(31)
	v_cvt_pk_f16_f32 v4, v96, v97
	v_cvt_pk_f16_f32 v5, v98, v99
	ds_write_b64 v144, v[4:5] offset:13056
	s_waitcnt vmcnt(30)
	v_cvt_pk_f16_f32 v4, v128, v129
	v_cvt_pk_f16_f32 v5, v130, v131
	ds_write_b64 v145, v[4:5] offset:13056
	global_load_dwordx4 v[96:99], v2, s[64:65] offset:3072 sc1 nt
	v_mov_b32_e32 v128, 0
	v_mov_b32_e32 v129, 0
	v_mov_b32_e32 v130, 0
	v_mov_b32_e32 v131, 0
	s_mov_b64 s[70:71], exec
	s_mov_b64 exec, s[68:69]
	global_load_dwordx4 v[128:131], v2, s[64:65] offset:3584 sc1 nt
	s_mov_b64 exec, s[70:71]
	s_waitcnt vmcnt(31)
	v_cvt_pk_f16_f32 v4, v100, v101
	v_cvt_pk_f16_f32 v5, v102, v103
	ds_write_b64 v144, v[4:5] offset:15232
	s_waitcnt vmcnt(30)
	v_cvt_pk_f16_f32 v4, v132, v133
	v_cvt_pk_f16_f32 v5, v134, v135
	ds_write_b64 v145, v[4:5] offset:15232
	global_load_dwordx4 v[100:103], v2, s[66:67] offset:3072 sc1 nt
	v_mov_b32_e32 v132, 0
	v_mov_b32_e32 v133, 0
	v_mov_b32_e32 v134, 0
	v_mov_b32_e32 v135, 0
	s_mov_b64 s[70:71], exec
	s_mov_b64 exec, s[68:69]
	global_load_dwordx4 v[132:135], v2, s[66:67] offset:3584 sc1 nt
	s_mov_b64 exec, s[70:71]
	s_waitcnt lgkmcnt(0)
	s_barrier
	s_waitcnt vmcnt(31)
	v_cvt_pk_f16_f32 v4, v8, v9
	v_cvt_pk_f16_f32 v5, v10, v11
	ds_write_b64 v141, v[4:5]
	s_waitcnt vmcnt(30)
	v_cvt_pk_f16_f32 v4, v40, v41
	v_cvt_pk_f16_f32 v5, v42, v43
	ds_write_b64 v142, v[4:5]
	s_waitcnt vmcnt(29)
	v_cvt_pk_f16_f32 v4, v12, v13
	v_cvt_pk_f16_f32 v5, v14, v15
	ds_write_b64 v141, v[4:5] offset:2176
	s_waitcnt vmcnt(28)
	v_cvt_pk_f16_f32 v4, v44, v45
	v_cvt_pk_f16_f32 v5, v46, v47
	ds_write_b64 v142, v[4:5] offset:2176
	s_waitcnt vmcnt(27)
	v_cvt_pk_f16_f32 v4, v16, v17
	v_cvt_pk_f16_f32 v5, v18, v19
	ds_write_b64 v141, v[4:5] offset:4352
	s_waitcnt vmcnt(26)
	v_cvt_pk_f16_f32 v4, v48, v49
	v_cvt_pk_f16_f32 v5, v50, v51
	ds_write_b64 v142, v[4:5] offset:4352
	s_waitcnt vmcnt(25)
	v_cvt_pk_f16_f32 v4, v20, v21
	v_cvt_pk_f16_f32 v5, v22, v23
	ds_write_b64 v141, v[4:5] offset:6528
	s_waitcnt vmcnt(24)
	v_cvt_pk_f16_f32 v4, v52, v53
	v_cvt_pk_f16_f32 v5, v54, v55
	ds_write_b64 v142, v[4:5] offset:6528
	s_waitcnt vmcnt(23)
	v_cvt_pk_f16_f32 v4, v24, v25
	v_cvt_pk_f16_f32 v5, v26, v27
	ds_write_b64 v141, v[4:5] offset:8704
	s_waitcnt vmcnt(22)
	v_cvt_pk_f16_f32 v4, v56, v57
	v_cvt_pk_f16_f32 v5, v58, v59
	ds_write_b64 v142, v[4:5] offset:8704
	s_waitcnt vmcnt(21)
	v_cvt_pk_f16_f32 v4, v28, v29
	v_cvt_pk_f16_f32 v5, v30, v31
	ds_write_b64 v141, v[4:5] offset:10880
	s_waitcnt vmcnt(20)
	v_cvt_pk_f16_f32 v4, v60, v61
	v_cvt_pk_f16_f32 v5, v62, v63
	ds_write_b64 v142, v[4:5] offset:10880
	s_waitcnt vmcnt(19)
	v_cvt_pk_f16_f32 v4, v32, v33
	v_cvt_pk_f16_f32 v5, v34, v35
	ds_write_b64 v141, v[4:5] offset:13056
	s_waitcnt vmcnt(18)
	v_cvt_pk_f16_f32 v4, v64, v65
	v_cvt_pk_f16_f32 v5, v66, v67
	ds_write_b64 v142, v[4:5] offset:13056
	s_waitcnt vmcnt(17)
	v_cvt_pk_f16_f32 v4, v36, v37
	v_cvt_pk_f16_f32 v5, v38, v39
	ds_write_b64 v141, v[4:5] offset:15232
	s_waitcnt vmcnt(16)
	v_cvt_pk_f16_f32 v4, v68, v69
	v_cvt_pk_f16_f32 v5, v70, v71
	ds_write_b64 v142, v[4:5] offset:15232
	s_waitcnt lgkmcnt(0)
	s_barrier
	s_waitcnt vmcnt(15)
	v_cvt_pk_f16_f32 v4, v72, v73
	v_cvt_pk_f16_f32 v5, v74, v75
	ds_write_b64 v143, v[4:5]
	s_waitcnt vmcnt(14)
	v_cvt_pk_f16_f32 v4, v104, v105
	v_cvt_pk_f16_f32 v5, v106, v107
	s_mov_b64 s[70:71], exec
	s_mov_b64 exec, s[78:79]
	ds_write_b64 v144, v[4:5]
	s_mov_b64 exec, s[70:71]
	s_waitcnt vmcnt(13)
	v_cvt_pk_f16_f32 v4, v76, v77
	v_cvt_pk_f16_f32 v5, v78, v79
	ds_write_b64 v143, v[4:5] offset:2176
	s_waitcnt vmcnt(12)
	v_cvt_pk_f16_f32 v4, v108, v109
	v_cvt_pk_f16_f32 v5, v110, v111
	s_mov_b64 s[70:71], exec
	s_mov_b64 exec, s[78:79]
	ds_write_b64 v144, v[4:5] offset:2176
	s_mov_b64 exec, s[70:71]
	s_waitcnt vmcnt(11)
	v_cvt_pk_f16_f32 v4, v80, v81
	v_cvt_pk_f16_f32 v5, v82, v83
	ds_write_b64 v143, v[4:5] offset:4352
	s_waitcnt vmcnt(10)
	v_cvt_pk_f16_f32 v4, v112, v113
	v_cvt_pk_f16_f32 v5, v114, v115
	s_mov_b64 s[70:71], exec
	s_mov_b64 exec, s[78:79]
	ds_write_b64 v144, v[4:5] offset:4352
	s_mov_b64 exec, s[70:71]
	s_waitcnt vmcnt(9)
	v_cvt_pk_f16_f32 v4, v84, v85
	v_cvt_pk_f16_f32 v5, v86, v87
	ds_write_b64 v143, v[4:5] offset:6528
	s_waitcnt vmcnt(8)
	v_cvt_pk_f16_f32 v4, v116, v117
	v_cvt_pk_f16_f32 v5, v118, v119
	s_mov_b64 s[70:71], exec
	s_mov_b64 exec, s[78:79]
	ds_write_b64 v144, v[4:5] offset:6528
	s_mov_b64 exec, s[70:71]
	s_waitcnt vmcnt(7)
	v_cvt_pk_f16_f32 v4, v88, v89
	v_cvt_pk_f16_f32 v5, v90, v91
	ds_write_b64 v143, v[4:5] offset:8704
	s_waitcnt vmcnt(6)
	v_cvt_pk_f16_f32 v4, v120, v121
	v_cvt_pk_f16_f32 v5, v122, v123
	s_mov_b64 s[70:71], exec
	s_mov_b64 exec, s[78:79]
	ds_write_b64 v144, v[4:5] offset:8704
	s_mov_b64 exec, s[70:71]
	s_waitcnt vmcnt(5)
	v_cvt_pk_f16_f32 v4, v92, v93
	v_cvt_pk_f16_f32 v5, v94, v95
	ds_write_b64 v143, v[4:5] offset:10880
	s_waitcnt vmcnt(4)
	v_cvt_pk_f16_f32 v4, v124, v125
	v_cvt_pk_f16_f32 v5, v126, v127
	s_mov_b64 s[70:71], exec
	s_mov_b64 exec, s[78:79]
	ds_write_b64 v144, v[4:5] offset:10880
	s_mov_b64 exec, s[70:71]
	s_waitcnt vmcnt(3)
	v_cvt_pk_f16_f32 v4, v96, v97
	v_cvt_pk_f16_f32 v5, v98, v99
	ds_write_b64 v143, v[4:5] offset:13056
	s_waitcnt vmcnt(2)
	v_cvt_pk_f16_f32 v4, v128, v129
	v_cvt_pk_f16_f32 v5, v130, v131
	s_mov_b64 s[70:71], exec
	s_mov_b64 exec, s[78:79]
	ds_write_b64 v144, v[4:5] offset:13056
	s_mov_b64 exec, s[70:71]
	s_waitcnt vmcnt(1)
	v_cvt_pk_f16_f32 v4, v100, v101
	v_cvt_pk_f16_f32 v5, v102, v103
	ds_write_b64 v143, v[4:5] offset:15232
	s_waitcnt vmcnt(0)
	v_cvt_pk_f16_f32 v4, v132, v133
	v_cvt_pk_f16_f32 v5, v134, v135
	s_mov_b64 s[70:71], exec
	s_mov_b64 exec, s[78:79]
	ds_write_b64 v144, v[4:5] offset:15232
	s_mov_b64 exec, s[70:71]
	s_waitcnt lgkmcnt(0)
	s_barrier
	s_barrier
	s_barrier
	s_endpgm
